# baseline (speedup 1.0000x reference)
.LBB3_35:
	s_andn2_b64 vcc, exec, s[2:3]
	s_cbranch_vccnz .LBB3_39
	s_waitcnt vmcnt(4)
	v_ashrrev_i32_e32 v81, 31, v80
	v_lshl_add_u64 v[2:3], v[80:81], 3, s[20:21]
	v_add_co_u32_e32 v2, vcc, 0x48000, v2
	s_movk_i32 s8, 0x620
	s_nop 0
	v_addc_co_u32_e32 v3, vcc, 0, v3, vcc
	global_load_dwordx2 v[82:83], v[2:3], off
	v_and_b32_e32 v2, 0x70, v7
	v_bitop3_b32 v2, v0, v2, 48 bitop3:0x6c
	s_waitcnt vmcnt(4)
	v_mad_u64_u32 v[64:65], s[6:7], v9, s8, v[2:3]
	v_lshrrev_b32_e32 v3, 4, v92
	v_bitop3_b32 v3, v3, v0, 4 bitop3:0x36
	v_lshlrev_b32_e32 v3, 4, v3
	v_and_b32_e32 v4, 0x70, v3
	s_waitcnt vmcnt(3)
	v_mad_u64_u32 v[66:67], s[6:7], v8, s8, v[4:5]
	s_waitcnt vmcnt(2)
	v_mad_u64_u32 v[68:69], s[6:7], v6, s8, v[2:3]
	s_waitcnt vmcnt(1)
	v_mad_u64_u32 v[70:71], s[6:7], v1, s8, v[4:5]
	v_lshrrev_b32_e32 v85, 5, v92
	v_bfe_u32 v2, v0, 1, 3
	s_mov_b64 s[6:7], 0x1800
	s_add_u32 s4, s20, 0x4000000
	v_bitop3_b32 v32, v85, v2, 2 bitop3:0x36
	v_bitop3_b32 v33, v85, v2, 4 bitop3:0x36
	v_bitop3_b32 v34, v85, v2, 6 bitop3:0x36
	v_lshl_add_u64 v[2:3], v[86:87], 0, s[6:7]
	s_addc_u32 s5, s21, 0
	s_lshl_b32 s2, s27, 12
	s_addk_i32 s2, 0x6000
	v_lshrrev_b32_e32 v1, 1, v0
	v_or_b32_e32 v81, s2, v84
	v_lshlrev_b32_e32 v0, 7, v0
	v_and_b32_e32 v8, 0xf80, v0
	v_lshlrev_b32_e32 v9, 4, v32
	v_bitop3_b32 v1, v85, v1, 7 bitop3:0x78
	v_or3_b32 v96, s2, v9, v8
	v_lshlrev_b32_e32 v9, 4, v33
	v_lshlrev_b32_e32 v1, 4, v1
	v_or3_b32 v97, s2, v9, v8
	v_lshlrev_b32_e32 v9, 4, v34
	v_or3_b32 v95, s2, v1, v8
	v_or3_b32 v94, s2, v9, v8
	v_add_u32_e32 v98, 0x103c0, v84
	global_load_dwordx4 v[116:119], v64, s[4:5] offset:0
	global_load_dwordx4 v[120:123], v66, s[4:5] offset:0
	global_load_dwordx4 v[124:127], v68, s[4:5] offset:0
	global_load_dwordx4 v[128:131], v70, s[4:5] offset:0
	global_load_dwordx4 v[132:135], v64, s[4:5] offset:128
	global_load_dwordx4 v[136:139], v66, s[4:5] offset:128
	global_load_dwordx4 v[140:143], v68, s[4:5] offset:128
	global_load_dwordx4 v[144:147], v70, s[4:5] offset:128
	global_load_dwordx4 v[148:151], v64, s[4:5] offset:256
	global_load_dwordx4 v[152:155], v66, s[4:5] offset:256
	global_load_dwordx4 v[156:159], v68, s[4:5] offset:256
	global_load_dwordx4 v[72:75], v70, s[4:5] offset:256
	s_add_u32 m0, s46, 0x0
	s_nop 0
	global_load_lds_dwordx4 v76, s[40:41]
	s_add_u32 m0, s47, 0x0
	s_nop 0
	global_load_lds_dwordx4 v77, s[42:43]
	s_add_u32 m0, s48, 0x0
	s_nop 0
	global_load_lds_dwordx4 v78, s[44:45]
	s_add_u32 m0, s46, 0x3000
	s_add_u32 s40, s40, 0x1800
	s_addc_u32 s41, s41, 0
	global_load_lds_dwordx4 v76, s[40:41]
	s_add_u32 m0, s47, 0x3000
	s_add_u32 s42, s42, 0x1800
	s_addc_u32 s43, s43, 0
	global_load_lds_dwordx4 v77, s[42:43]
	s_add_u32 m0, s48, 0x3000
	s_add_u32 s44, s44, 0x1800
	s_addc_u32 s45, s45, 0
	global_load_lds_dwordx4 v78, s[44:45]
	s_add_u32 m0, s46, 0xd3c0
	s_add_u32 s40, s40, 0x1800
	s_addc_u32 s41, s41, 0
	global_load_lds_dwordx4 v76, s[40:41]
	s_add_u32 m0, s47, 0xd3c0
	s_add_u32 s42, s42, 0x1800
	s_addc_u32 s43, s43, 0
	global_load_lds_dwordx4 v77, s[42:43]
	s_add_u32 m0, s48, 0xd3c0
	s_add_u32 s44, s44, 0x1800
	s_addc_u32 s45, s45, 0
	global_load_lds_dwordx4 v78, s[44:45]
	s_add_u32 m0, s46, 0x103c0
	s_add_u32 s40, s40, 0x1800
	s_addc_u32 s41, s41, 0
	global_load_lds_dwordx4 v76, s[40:41]
	s_add_u32 m0, s47, 0x103c0
	s_add_u32 s42, s42, 0x1800
	s_addc_u32 s43, s43, 0
	global_load_lds_dwordx4 v77, s[42:43]
	s_add_u32 m0, s48, 0x103c0
	s_add_u32 s44, s44, 0x1800
	s_addc_u32 s45, s45, 0
	global_load_lds_dwordx4 v78, s[44:45]
	s_waitcnt vmcnt(20)
	ds_write_b128 v81, v[116:119]
	ds_write_b128 v81, v[120:123] offset:1024
	ds_write_b128 v81, v[124:127] offset:2048
	ds_write_b128 v81, v[128:131] offset:3072
	ds_read_b128 v[52:55], v95
	ds_read_b128 v[56:59], v96
	ds_read_b128 v[60:63], v97
	ds_read_b128 v[0:3], v94
	global_load_dwordx4 v[116:119], v64, s[4:5] offset:384
	global_load_dwordx4 v[120:123], v66, s[4:5] offset:384
	global_load_dwordx4 v[124:127], v68, s[4:5] offset:384
	global_load_dwordx4 v[128:131], v70, s[4:5] offset:384
	s_waitcnt vmcnt(13)
	s_waitcnt lgkmcnt(0)
	s_barrier
	ds_read_b128 v[4:7], v84 offset:0
	ds_read_b128 v[8:11], v84 offset:1024
	ds_read_b128 v[12:15], v84 offset:2048
	ds_read_b128 v[16:19], v84 offset:3072
	ds_read_b128 v[20:23], v84 offset:4096
	ds_read_b128 v[24:27], v84 offset:5120
	ds_read_b128 v[28:31], v84 offset:6144
	ds_read_b128 v[32:35], v84 offset:7168
	ds_read_b128 v[36:39], v84 offset:8192
	ds_read_b128 v[40:43], v84 offset:9216
	ds_read_b128 v[44:47], v84 offset:10240
	ds_read_b128 v[48:51], v84 offset:11264
	s_waitcnt lgkmcnt(11)
	v_mfma_f32_32x32x16_f16 a[80:95], v[4:7], v[52:55], 0
	s_waitcnt lgkmcnt(10)
	v_mfma_f32_32x32x16_f16 a[64:79], v[8:11], v[52:55], 0
	s_waitcnt lgkmcnt(9)
	v_mfma_f32_32x32x16_f16 a[48:63], v[12:15], v[52:55], 0
	s_waitcnt lgkmcnt(8)
	v_mfma_f32_32x32x16_f16 a[32:47], v[16:19], v[52:55], 0
	s_waitcnt lgkmcnt(7)
	v_mfma_f32_32x32x16_f16 a[16:31], v[20:23], v[52:55], 0
	s_waitcnt lgkmcnt(6)
	v_mfma_f32_32x32x16_f16 a[0:15], v[24:27], v[52:55], 0
	s_waitcnt vmcnt(10)
	s_waitcnt lgkmcnt(0)
	s_barrier
	v_mfma_f32_32x32x16_f16 a[80:95], v[28:31], v[56:59], a[80:95]
	ds_read_b128 v[4:7], v84 offset:12288
	ds_read_b128 v[28:31], v84 offset:18432
	s_add_u32 m0, s46, 0x0
	s_add_u32 s40, s40, 0x1800
	s_addc_u32 s41, s41, 0
	global_load_lds_dwordx4 v76, s[40:41]
	v_mfma_f32_32x32x16_f16 a[64:79], v[32:35], v[56:59], a[64:79]
	ds_read_b128 v[8:11], v84 offset:13312
	ds_read_b128 v[32:35], v84 offset:19456
	v_mfma_f32_32x32x16_f16 a[48:63], v[36:39], v[56:59], a[48:63]
	ds_read_b128 v[12:15], v84 offset:14336
	ds_read_b128 v[36:39], v84 offset:20480
	s_add_u32 m0, s47, 0x0
	s_add_u32 s42, s42, 0x1800
	s_addc_u32 s43, s43, 0
	global_load_lds_dwordx4 v77, s[42:43]
	v_mfma_f32_32x32x16_f16 a[32:47], v[40:43], v[56:59], a[32:47]
	ds_read_b128 v[16:19], v84 offset:15360
	ds_read_b128 v[40:43], v84 offset:21504
	v_mfma_f32_32x32x16_f16 a[16:31], v[44:47], v[56:59], a[16:31]
	ds_read_b128 v[20:23], v84 offset:16384
	ds_read_b128 v[44:47], v84 offset:22528
	s_add_u32 m0, s48, 0x0
	s_add_u32 s44, s44, 0x1800
	s_addc_u32 s45, s45, 0
	global_load_lds_dwordx4 v78, s[44:45]
	v_mfma_f32_32x32x16_f16 a[0:15], v[48:51], v[56:59], a[0:15]
	ds_read_b128 v[24:27], v84 offset:17408
	ds_read_b128 v[48:51], v84 offset:23552
	s_waitcnt lgkmcnt(11)
	v_mfma_f32_32x32x16_f16 a[80:95], v[4:7], v[60:63], a[80:95]
	s_waitcnt vmcnt(23)
	ds_write_b128 v81, v[132:135]
	ds_write_b128 v81, v[136:139] offset:1024
	ds_write_b128 v81, v[140:143] offset:2048
	ds_write_b128 v81, v[144:147] offset:3072
	s_waitcnt lgkmcnt(13)
	v_mfma_f32_32x32x16_f16 a[64:79], v[8:11], v[60:63], a[64:79]
	ds_read_b128 v[100:103], v95
	ds_read_b128 v[104:107], v96
	s_waitcnt lgkmcnt(14)
	ds_read_b128 v[108:111], v97
	s_waitcnt lgkmcnt(14)
	ds_read_b128 v[112:115], v94
	v_mfma_f32_32x32x16_f16 a[48:63], v[12:15], v[60:63], a[48:63]
	global_load_dwordx4 v[132:135], v64, s[4:5] offset:512
	global_load_dwordx4 v[136:139], v66, s[4:5] offset:512
	global_load_dwordx4 v[140:143], v68, s[4:5] offset:512
	global_load_dwordx4 v[144:147], v70, s[4:5] offset:512
	s_waitcnt lgkmcnt(13)
	v_mfma_f32_32x32x16_f16 a[32:47], v[16:19], v[60:63], a[32:47]
	s_waitcnt lgkmcnt(11)
	v_mfma_f32_32x32x16_f16 a[16:31], v[20:23], v[60:63], a[16:31]
	s_waitcnt lgkmcnt(9)
	v_mfma_f32_32x32x16_f16 a[0:15], v[24:27], v[60:63], a[0:15]
	s_waitcnt vmcnt(14)
	s_waitcnt lgkmcnt(0)
	s_barrier
	v_mfma_f32_32x32x16_f16 a[80:95], v[28:31], v[0:3], a[80:95]
	ds_read_b128 v[4:7], v84 offset:54208
	ds_read_b128 v[28:31], v84 offset:60352
	s_add_u32 m0, s46, 0x3000
	s_add_u32 s40, s40, 0x1800
	s_addc_u32 s41, s41, 0
	global_load_lds_dwordx4 v76, s[40:41]
	v_mfma_f32_32x32x16_f16 a[64:79], v[32:35], v[0:3], a[64:79]
	ds_read_b128 v[8:11], v84 offset:55232
	ds_read_b128 v[32:35], v84 offset:61376
	v_mfma_f32_32x32x16_f16 a[48:63], v[36:39], v[0:3], a[48:63]
	ds_read_b128 v[12:15], v84 offset:56256
	ds_read_b128 v[36:39], v84 offset:62400
	s_add_u32 m0, s47, 0x3000
	s_add_u32 s42, s42, 0x1800
	s_addc_u32 s43, s43, 0
	global_load_lds_dwordx4 v77, s[42:43]
	v_mfma_f32_32x32x16_f16 a[32:47], v[40:43], v[0:3], a[32:47]
	ds_read_b128 v[16:19], v84 offset:57280
	ds_read_b128 v[40:43], v84 offset:63424
	v_mfma_f32_32x32x16_f16 a[16:31], v[44:47], v[0:3], a[16:31]
	ds_read_b128 v[20:23], v84 offset:58304
	ds_read_b128 v[44:47], v84 offset:64448
	s_add_u32 m0, s48, 0x3000
	s_add_u32 s44, s44, 0x1800
	s_addc_u32 s45, s45, 0
	global_load_lds_dwordx4 v78, s[44:45]
	v_mfma_f32_32x32x16_f16 a[0:15], v[48:51], v[0:3], a[0:15]
	ds_read_b128 v[24:27], v84 offset:59328
	ds_read_b128 v[48:51], v84 offset:65472
	s_waitcnt lgkmcnt(11)
	v_mfma_f32_32x32x16_f16 a[80:95], v[4:7], v[100:103], a[80:95]
	s_waitcnt lgkmcnt(9)
	v_mfma_f32_32x32x16_f16 a[64:79], v[8:11], v[100:103], a[64:79]
	s_waitcnt lgkmcnt(7)
	v_mfma_f32_32x32x16_f16 a[48:63], v[12:15], v[100:103], a[48:63]
	s_waitcnt lgkmcnt(5)
	v_mfma_f32_32x32x16_f16 a[32:47], v[16:19], v[100:103], a[32:47]
	s_waitcnt lgkmcnt(3)
	v_mfma_f32_32x32x16_f16 a[16:31], v[20:23], v[100:103], a[16:31]
	s_waitcnt lgkmcnt(1)
	v_mfma_f32_32x32x16_f16 a[0:15], v[24:27], v[100:103], a[0:15]
	s_waitcnt vmcnt(14)
	s_waitcnt lgkmcnt(0)
	s_barrier
	v_mfma_f32_32x32x16_f16 a[80:95], v[28:31], v[104:107], a[80:95]
	ds_read_b128 v[4:7], v98
	ds_read_b128 v[28:31], v98 offset:6144
	s_add_u32 m0, s46, 0xd3c0
	s_add_u32 s40, s40, 0x1800
	s_addc_u32 s41, s41, 0
	global_load_lds_dwordx4 v76, s[40:41]
	v_mfma_f32_32x32x16_f16 a[64:79], v[32:35], v[104:107], a[64:79]
	ds_read_b128 v[8:11], v98 offset:1024
	ds_read_b128 v[32:35], v98 offset:7168
	v_mfma_f32_32x32x16_f16 a[48:63], v[36:39], v[104:107], a[48:63]
	ds_read_b128 v[12:15], v98 offset:2048
	ds_read_b128 v[36:39], v98 offset:8192
	s_add_u32 m0, s47, 0xd3c0
	s_add_u32 s42, s42, 0x1800
	s_addc_u32 s43, s43, 0
	global_load_lds_dwordx4 v77, s[42:43]
	v_mfma_f32_32x32x16_f16 a[32:47], v[40:43], v[104:107], a[32:47]
	ds_read_b128 v[16:19], v98 offset:3072
	ds_read_b128 v[40:43], v98 offset:9216
	v_mfma_f32_32x32x16_f16 a[16:31], v[44:47], v[104:107], a[16:31]
	ds_read_b128 v[20:23], v98 offset:4096
	ds_read_b128 v[44:47], v98 offset:10240
	s_add_u32 m0, s48, 0xd3c0
	s_add_u32 s44, s44, 0x1800
	s_addc_u32 s45, s45, 0
	global_load_lds_dwordx4 v78, s[44:45]
	v_mfma_f32_32x32x16_f16 a[0:15], v[48:51], v[104:107], a[0:15]
	ds_read_b128 v[24:27], v98 offset:5120
	ds_read_b128 v[48:51], v98 offset:11264
	s_waitcnt lgkmcnt(11)
	v_mfma_f32_32x32x16_f16 a[80:95], v[4:7], v[108:111], a[80:95]
	s_waitcnt vmcnt(29)
	ds_write_b128 v81, v[148:151]
	ds_write_b128 v81, v[152:155] offset:1024
	ds_write_b128 v81, v[156:159] offset:2048
	ds_write_b128 v81, v[72:75] offset:3072
	s_waitcnt lgkmcnt(13)
	v_mfma_f32_32x32x16_f16 a[64:79], v[8:11], v[108:111], a[64:79]
	ds_read_b128 v[52:55], v95
	ds_read_b128 v[56:59], v96
	s_waitcnt lgkmcnt(14)
	ds_read_b128 v[60:63], v97
	s_waitcnt lgkmcnt(14)
	ds_read_b128 v[0:3], v94
	v_mfma_f32_32x32x16_f16 a[48:63], v[12:15], v[108:111], a[48:63]
	global_load_dwordx4 v[148:151], v64, s[4:5] offset:640
	global_load_dwordx4 v[152:155], v66, s[4:5] offset:640
	global_load_dwordx4 v[156:159], v68, s[4:5] offset:640
	global_load_dwordx4 v[72:75], v70, s[4:5] offset:640
	s_waitcnt lgkmcnt(13)
	v_mfma_f32_32x32x16_f16 a[32:47], v[16:19], v[108:111], a[32:47]
	s_waitcnt lgkmcnt(11)
	v_mfma_f32_32x32x16_f16 a[16:31], v[20:23], v[108:111], a[16:31]
	s_waitcnt lgkmcnt(9)
	v_mfma_f32_32x32x16_f16 a[0:15], v[24:27], v[108:111], a[0:15]
	s_waitcnt vmcnt(14)
	s_waitcnt lgkmcnt(0)
	s_barrier
	v_mfma_f32_32x32x16_f16 a[80:95], v[28:31], v[112:115], a[80:95]
	ds_read_b128 v[4:7], v84 offset:0
	ds_read_b128 v[28:31], v84 offset:6144
	s_add_u32 m0, s46, 0x103c0
	s_add_u32 s40, s40, 0x1800
	s_addc_u32 s41, s41, 0
	global_load_lds_dwordx4 v76, s[40:41]
	v_mfma_f32_32x32x16_f16 a[64:79], v[32:35], v[112:115], a[64:79]
	ds_read_b128 v[8:11], v84 offset:1024
	ds_read_b128 v[32:35], v84 offset:7168
	v_mfma_f32_32x32x16_f16 a[48:63], v[36:39], v[112:115], a[48:63]
	ds_read_b128 v[12:15], v84 offset:2048
	ds_read_b128 v[36:39], v84 offset:8192
	s_add_u32 m0, s47, 0x103c0
	s_add_u32 s42, s42, 0x1800
	s_addc_u32 s43, s43, 0
	global_load_lds_dwordx4 v77, s[42:43]
	v_mfma_f32_32x32x16_f16 a[32:47], v[40:43], v[112:115], a[32:47]
	ds_read_b128 v[16:19], v84 offset:3072
	ds_read_b128 v[40:43], v84 offset:9216
	v_mfma_f32_32x32x16_f16 a[16:31], v[44:47], v[112:115], a[16:31]
	ds_read_b128 v[20:23], v84 offset:4096
	ds_read_b128 v[44:47], v84 offset:10240
	s_add_u32 m0, s48, 0x103c0
	s_add_u32 s44, s44, 0x1800
	s_addc_u32 s45, s45, 0
	global_load_lds_dwordx4 v78, s[44:45]
	v_mfma_f32_32x32x16_f16 a[0:15], v[48:51], v[112:115], a[0:15]
	ds_read_b128 v[24:27], v84 offset:5120
	ds_read_b128 v[48:51], v84 offset:11264
	s_waitcnt lgkmcnt(11)
	v_mfma_f32_32x32x16_f16 a[80:95], v[4:7], v[52:55], a[80:95]
	s_waitcnt lgkmcnt(9)
	v_mfma_f32_32x32x16_f16 a[64:79], v[8:11], v[52:55], a[64:79]
	s_waitcnt lgkmcnt(7)
	v_mfma_f32_32x32x16_f16 a[48:63], v[12:15], v[52:55], a[48:63]
	s_waitcnt lgkmcnt(5)
	v_mfma_f32_32x32x16_f16 a[32:47], v[16:19], v[52:55], a[32:47]
	s_waitcnt lgkmcnt(3)
	v_mfma_f32_32x32x16_f16 a[16:31], v[20:23], v[52:55], a[16:31]
	s_waitcnt lgkmcnt(1)
	v_mfma_f32_32x32x16_f16 a[0:15], v[24:27], v[52:55], a[0:15]
	s_waitcnt vmcnt(10)
	s_waitcnt lgkmcnt(0)
	s_barrier
	v_mfma_f32_32x32x16_f16 a[80:95], v[28:31], v[56:59], a[80:95]
	ds_read_b128 v[4:7], v84 offset:12288
	ds_read_b128 v[28:31], v84 offset:18432
	s_add_u32 m0, s46, 0x0
	s_add_u32 s40, s40, 0x1800
	s_addc_u32 s41, s41, 0
	global_load_lds_dwordx4 v76, s[40:41]
	v_mfma_f32_32x32x16_f16 a[64:79], v[32:35], v[56:59], a[64:79]
	ds_read_b128 v[8:11], v84 offset:13312
	ds_read_b128 v[32:35], v84 offset:19456
	v_mfma_f32_32x32x16_f16 a[48:63], v[36:39], v[56:59], a[48:63]
	ds_read_b128 v[12:15], v84 offset:14336
	ds_read_b128 v[36:39], v84 offset:20480
	s_add_u32 m0, s47, 0x0
	s_add_u32 s42, s42, 0x1800
	s_addc_u32 s43, s43, 0
	global_load_lds_dwordx4 v77, s[42:43]
	v_mfma_f32_32x32x16_f16 a[32:47], v[40:43], v[56:59], a[32:47]
	ds_read_b128 v[16:19], v84 offset:15360
	ds_read_b128 v[40:43], v84 offset:21504
	v_mfma_f32_32x32x16_f16 a[16:31], v[44:47], v[56:59], a[16:31]
	ds_read_b128 v[20:23], v84 offset:16384
	ds_read_b128 v[44:47], v84 offset:22528
	s_add_u32 m0, s48, 0x0
	s_add_u32 s44, s44, 0x1800
	s_addc_u32 s45, s45, 0
	global_load_lds_dwordx4 v78, s[44:45]
	v_mfma_f32_32x32x16_f16 a[0:15], v[48:51], v[56:59], a[0:15]
	ds_read_b128 v[24:27], v84 offset:17408
	ds_read_b128 v[48:51], v84 offset:23552
	s_waitcnt lgkmcnt(11)
	v_mfma_f32_32x32x16_f16 a[80:95], v[4:7], v[60:63], a[80:95]
	s_waitcnt vmcnt(23)
	ds_write_b128 v81, v[116:119]
	ds_write_b128 v81, v[120:123] offset:1024
	ds_write_b128 v81, v[124:127] offset:2048
	ds_write_b128 v81, v[128:131] offset:3072
	s_waitcnt lgkmcnt(13)
	v_mfma_f32_32x32x16_f16 a[64:79], v[8:11], v[60:63], a[64:79]
	ds_read_b128 v[100:103], v95
	ds_read_b128 v[104:107], v96
	s_waitcnt lgkmcnt(14)
	ds_read_b128 v[108:111], v97
	s_waitcnt lgkmcnt(14)
	ds_read_b128 v[112:115], v94
	v_mfma_f32_32x32x16_f16 a[48:63], v[12:15], v[60:63], a[48:63]
	global_load_dwordx4 v[116:119], v64, s[4:5] offset:768
	global_load_dwordx4 v[120:123], v66, s[4:5] offset:768
	global_load_dwordx4 v[124:127], v68, s[4:5] offset:768
	global_load_dwordx4 v[128:131], v70, s[4:5] offset:768
	s_waitcnt lgkmcnt(13)
	v_mfma_f32_32x32x16_f16 a[32:47], v[16:19], v[60:63], a[32:47]
	s_waitcnt lgkmcnt(11)
	v_mfma_f32_32x32x16_f16 a[16:31], v[20:23], v[60:63], a[16:31]
	s_waitcnt lgkmcnt(9)
	v_mfma_f32_32x32x16_f16 a[0:15], v[24:27], v[60:63], a[0:15]
	s_waitcnt vmcnt(14)
	s_waitcnt lgkmcnt(0)
	s_barrier
	v_mfma_f32_32x32x16_f16 a[80:95], v[28:31], v[0:3], a[80:95]
	ds_read_b128 v[4:7], v84 offset:54208
	ds_read_b128 v[28:31], v84 offset:60352
	s_add_u32 m0, s46, 0x3000
	s_add_u32 s40, s40, 0x1800
	s_addc_u32 s41, s41, 0
	global_load_lds_dwordx4 v76, s[40:41]
	v_mfma_f32_32x32x16_f16 a[64:79], v[32:35], v[0:3], a[64:79]
	ds_read_b128 v[8:11], v84 offset:55232
	ds_read_b128 v[32:35], v84 offset:61376
	v_mfma_f32_32x32x16_f16 a[48:63], v[36:39], v[0:3], a[48:63]
	ds_read_b128 v[12:15], v84 offset:56256
	ds_read_b128 v[36:39], v84 offset:62400
	s_add_u32 m0, s47, 0x3000
	s_add_u32 s42, s42, 0x1800
	s_addc_u32 s43, s43, 0
	global_load_lds_dwordx4 v77, s[42:43]
	v_mfma_f32_32x32x16_f16 a[32:47], v[40:43], v[0:3], a[32:47]
	ds_read_b128 v[16:19], v84 offset:57280
	ds_read_b128 v[40:43], v84 offset:63424
	v_mfma_f32_32x32x16_f16 a[16:31], v[44:47], v[0:3], a[16:31]
	ds_read_b128 v[20:23], v84 offset:58304
	ds_read_b128 v[44:47], v84 offset:64448
	s_add_u32 m0, s48, 0x3000
	s_add_u32 s44, s44, 0x1800
	s_addc_u32 s45, s45, 0
	global_load_lds_dwordx4 v78, s[44:45]
	v_mfma_f32_32x32x16_f16 a[0:15], v[48:51], v[0:3], a[0:15]
	ds_read_b128 v[24:27], v84 offset:59328
	ds_read_b128 v[48:51], v84 offset:65472
	s_waitcnt lgkmcnt(11)
	v_mfma_f32_32x32x16_f16 a[80:95], v[4:7], v[100:103], a[80:95]
	s_waitcnt lgkmcnt(9)
	v_mfma_f32_32x32x16_f16 a[64:79], v[8:11], v[100:103], a[64:79]
	s_waitcnt lgkmcnt(7)
	v_mfma_f32_32x32x16_f16 a[48:63], v[12:15], v[100:103], a[48:63]
	s_waitcnt lgkmcnt(5)
	v_mfma_f32_32x32x16_f16 a[32:47], v[16:19], v[100:103], a[32:47]
	s_waitcnt lgkmcnt(3)
	v_mfma_f32_32x32x16_f16 a[16:31], v[20:23], v[100:103], a[16:31]
	s_waitcnt lgkmcnt(1)
	v_mfma_f32_32x32x16_f16 a[0:15], v[24:27], v[100:103], a[0:15]
	s_waitcnt vmcnt(10)
	s_waitcnt lgkmcnt(0)
	s_barrier
	v_mfma_f32_32x32x16_f16 a[80:95], v[28:31], v[104:107], a[80:95]
	ds_read_b128 v[4:7], v98
	ds_read_b128 v[28:31], v98 offset:6144
	s_add_u32 m0, s46, 0xd3c0
	s_add_u32 s40, s40, 0x1800
	s_addc_u32 s41, s41, 0
	global_load_lds_dwordx4 v76, s[40:41]
	v_mfma_f32_32x32x16_f16 a[64:79], v[32:35], v[104:107], a[64:79]
	ds_read_b128 v[8:11], v98 offset:1024
	ds_read_b128 v[32:35], v98 offset:7168
	v_mfma_f32_32x32x16_f16 a[48:63], v[36:39], v[104:107], a[48:63]
	ds_read_b128 v[12:15], v98 offset:2048
	ds_read_b128 v[36:39], v98 offset:8192
	s_add_u32 m0, s47, 0xd3c0
	s_add_u32 s42, s42, 0x1800
	s_addc_u32 s43, s43, 0
	global_load_lds_dwordx4 v77, s[42:43]
	v_mfma_f32_32x32x16_f16 a[32:47], v[40:43], v[104:107], a[32:47]
	ds_read_b128 v[16:19], v98 offset:3072
	ds_read_b128 v[40:43], v98 offset:9216
	v_mfma_f32_32x32x16_f16 a[16:31], v[44:47], v[104:107], a[16:31]
	ds_read_b128 v[20:23], v98 offset:4096
	ds_read_b128 v[44:47], v98 offset:10240
	s_add_u32 m0, s48, 0xd3c0
	s_add_u32 s44, s44, 0x1800
	s_addc_u32 s45, s45, 0
	global_load_lds_dwordx4 v78, s[44:45]
	v_mfma_f32_32x32x16_f16 a[0:15], v[48:51], v[104:107], a[0:15]
	ds_read_b128 v[24:27], v98 offset:5120
	ds_read_b128 v[48:51], v98 offset:11264
	s_waitcnt lgkmcnt(11)
	v_mfma_f32_32x32x16_f16 a[80:95], v[4:7], v[108:111], a[80:95]
	s_waitcnt vmcnt(26)
	ds_write_b128 v81, v[132:135]
	ds_write_b128 v81, v[136:139] offset:1024
	ds_write_b128 v81, v[140:143] offset:2048
	ds_write_b128 v81, v[144:147] offset:3072
	s_waitcnt lgkmcnt(13)
	v_mfma_f32_32x32x16_f16 a[64:79], v[8:11], v[108:111], a[64:79]
	ds_read_b128 v[52:55], v95
	ds_read_b128 v[56:59], v96
	s_waitcnt lgkmcnt(14)
	ds_read_b128 v[60:63], v97
	s_waitcnt lgkmcnt(14)
	ds_read_b128 v[0:3], v94
	v_mfma_f32_32x32x16_f16 a[48:63], v[12:15], v[108:111], a[48:63]
	global_load_dwordx4 v[132:135], v64, s[4:5] offset:896
	global_load_dwordx4 v[136:139], v66, s[4:5] offset:896
	global_load_dwordx4 v[140:143], v68, s[4:5] offset:896
	global_load_dwordx4 v[144:147], v70, s[4:5] offset:896
	s_waitcnt lgkmcnt(13)
	v_mfma_f32_32x32x16_f16 a[32:47], v[16:19], v[108:111], a[32:47]
	s_waitcnt lgkmcnt(11)
	v_mfma_f32_32x32x16_f16 a[16:31], v[20:23], v[108:111], a[16:31]
	s_waitcnt lgkmcnt(9)
	v_mfma_f32_32x32x16_f16 a[0:15], v[24:27], v[108:111], a[0:15]
	s_waitcnt vmcnt(14)
	s_waitcnt lgkmcnt(0)
	s_barrier
	v_mfma_f32_32x32x16_f16 a[80:95], v[28:31], v[112:115], a[80:95]
	ds_read_b128 v[4:7], v84 offset:0
	ds_read_b128 v[28:31], v84 offset:6144
	s_add_u32 m0, s46, 0x103c0
	s_add_u32 s40, s40, 0x1800
	s_addc_u32 s41, s41, 0
	global_load_lds_dwordx4 v76, s[40:41]
	v_mfma_f32_32x32x16_f16 a[64:79], v[32:35], v[112:115], a[64:79]
	ds_read_b128 v[8:11], v84 offset:1024
	ds_read_b128 v[32:35], v84 offset:7168
	v_mfma_f32_32x32x16_f16 a[48:63], v[36:39], v[112:115], a[48:63]
	ds_read_b128 v[12:15], v84 offset:2048
	ds_read_b128 v[36:39], v84 offset:8192
	s_add_u32 m0, s47, 0x103c0
	s_add_u32 s42, s42, 0x1800
	s_addc_u32 s43, s43, 0
	global_load_lds_dwordx4 v77, s[42:43]
	v_mfma_f32_32x32x16_f16 a[32:47], v[40:43], v[112:115], a[32:47]
	ds_read_b128 v[16:19], v84 offset:3072
	ds_read_b128 v[40:43], v84 offset:9216
	v_mfma_f32_32x32x16_f16 a[16:31], v[44:47], v[112:115], a[16:31]
	ds_read_b128 v[20:23], v84 offset:4096
	ds_read_b128 v[44:47], v84 offset:10240
	s_add_u32 m0, s48, 0x103c0
	s_add_u32 s44, s44, 0x1800
	s_addc_u32 s45, s45, 0
	global_load_lds_dwordx4 v78, s[44:45]
	v_mfma_f32_32x32x16_f16 a[0:15], v[48:51], v[112:115], a[0:15]
	ds_read_b128 v[24:27], v84 offset:5120
	ds_read_b128 v[48:51], v84 offset:11264
	s_waitcnt lgkmcnt(11)
	v_mfma_f32_32x32x16_f16 a[80:95], v[4:7], v[52:55], a[80:95]
	s_waitcnt lgkmcnt(9)
	v_mfma_f32_32x32x16_f16 a[64:79], v[8:11], v[52:55], a[64:79]
	s_waitcnt lgkmcnt(7)
	v_mfma_f32_32x32x16_f16 a[48:63], v[12:15], v[52:55], a[48:63]
	s_waitcnt lgkmcnt(5)
	v_mfma_f32_32x32x16_f16 a[32:47], v[16:19], v[52:55], a[32:47]
	s_waitcnt lgkmcnt(3)
	v_mfma_f32_32x32x16_f16 a[16:31], v[20:23], v[52:55], a[16:31]
	s_waitcnt lgkmcnt(1)
	v_mfma_f32_32x32x16_f16 a[0:15], v[24:27], v[52:55], a[0:15]
	s_waitcnt vmcnt(10)
	s_waitcnt lgkmcnt(0)
	s_barrier
	v_mfma_f32_32x32x16_f16 a[80:95], v[28:31], v[56:59], a[80:95]
	ds_read_b128 v[4:7], v84 offset:12288
	ds_read_b128 v[28:31], v84 offset:18432
	s_add_u32 m0, s46, 0x0
	s_add_u32 s40, s40, 0x1800
	s_addc_u32 s41, s41, 0
	global_load_lds_dwordx4 v76, s[40:41]
	v_mfma_f32_32x32x16_f16 a[64:79], v[32:35], v[56:59], a[64:79]
	ds_read_b128 v[8:11], v84 offset:13312
	ds_read_b128 v[32:35], v84 offset:19456
	v_mfma_f32_32x32x16_f16 a[48:63], v[36:39], v[56:59], a[48:63]
	ds_read_b128 v[12:15], v84 offset:14336
	ds_read_b128 v[36:39], v84 offset:20480
	s_add_u32 m0, s47, 0x0
	s_add_u32 s42, s42, 0x1800
	s_addc_u32 s43, s43, 0
	global_load_lds_dwordx4 v77, s[42:43]
	v_mfma_f32_32x32x16_f16 a[32:47], v[40:43], v[56:59], a[32:47]
	ds_read_b128 v[16:19], v84 offset:15360
	ds_read_b128 v[40:43], v84 offset:21504
	v_mfma_f32_32x32x16_f16 a[16:31], v[44:47], v[56:59], a[16:31]
	ds_read_b128 v[20:23], v84 offset:16384
	ds_read_b128 v[44:47], v84 offset:22528
	s_add_u32 m0, s48, 0x0
	s_add_u32 s44, s44, 0x1800
	s_addc_u32 s45, s45, 0
	global_load_lds_dwordx4 v78, s[44:45]
	v_mfma_f32_32x32x16_f16 a[0:15], v[48:51], v[56:59], a[0:15]
	ds_read_b128 v[24:27], v84 offset:17408
	ds_read_b128 v[48:51], v84 offset:23552
	s_waitcnt lgkmcnt(11)
	v_mfma_f32_32x32x16_f16 a[80:95], v[4:7], v[60:63], a[80:95]
	s_waitcnt vmcnt(26)
	ds_write_b128 v81, v[148:151]
	ds_write_b128 v81, v[152:155] offset:1024
	ds_write_b128 v81, v[156:159] offset:2048
	ds_write_b128 v81, v[72:75] offset:3072
	s_waitcnt lgkmcnt(13)
	v_mfma_f32_32x32x16_f16 a[64:79], v[8:11], v[60:63], a[64:79]
	ds_read_b128 v[100:103], v95
	ds_read_b128 v[104:107], v96
	s_waitcnt lgkmcnt(14)
	ds_read_b128 v[108:111], v97
	s_waitcnt lgkmcnt(14)
	ds_read_b128 v[112:115], v94
	v_mfma_f32_32x32x16_f16 a[48:63], v[12:15], v[60:63], a[48:63]
	global_load_dwordx4 v[148:151], v64, s[4:5] offset:1024
	global_load_dwordx4 v[152:155], v66, s[4:5] offset:1024
	global_load_dwordx4 v[156:159], v68, s[4:5] offset:1024
	global_load_dwordx4 v[72:75], v70, s[4:5] offset:1024
	s_waitcnt lgkmcnt(13)
	v_mfma_f32_32x32x16_f16 a[32:47], v[16:19], v[60:63], a[32:47]
	s_waitcnt lgkmcnt(11)
	v_mfma_f32_32x32x16_f16 a[16:31], v[20:23], v[60:63], a[16:31]
	s_waitcnt lgkmcnt(9)
	v_mfma_f32_32x32x16_f16 a[0:15], v[24:27], v[60:63], a[0:15]
	s_waitcnt vmcnt(14)
	s_waitcnt lgkmcnt(0)
	s_barrier
	v_mfma_f32_32x32x16_f16 a[80:95], v[28:31], v[0:3], a[80:95]
	ds_read_b128 v[4:7], v84 offset:54208
	ds_read_b128 v[28:31], v84 offset:60352
	s_add_u32 m0, s46, 0x3000
	s_add_u32 s40, s40, 0x1800
	s_addc_u32 s41, s41, 0
	global_load_lds_dwordx4 v76, s[40:41]
	v_mfma_f32_32x32x16_f16 a[64:79], v[32:35], v[0:3], a[64:79]
	ds_read_b128 v[8:11], v84 offset:55232
	ds_read_b128 v[32:35], v84 offset:61376
	v_mfma_f32_32x32x16_f16 a[48:63], v[36:39], v[0:3], a[48:63]
	ds_read_b128 v[12:15], v84 offset:56256
	ds_read_b128 v[36:39], v84 offset:62400
	s_add_u32 m0, s47, 0x3000
	s_add_u32 s42, s42, 0x1800
	s_addc_u32 s43, s43, 0
	global_load_lds_dwordx4 v77, s[42:43]
	v_mfma_f32_32x32x16_f16 a[32:47], v[40:43], v[0:3], a[32:47]
	ds_read_b128 v[16:19], v84 offset:57280
	ds_read_b128 v[40:43], v84 offset:63424
	v_mfma_f32_32x32x16_f16 a[16:31], v[44:47], v[0:3], a[16:31]
	ds_read_b128 v[20:23], v84 offset:58304
	ds_read_b128 v[44:47], v84 offset:64448
	s_add_u32 m0, s48, 0x3000
	s_add_u32 s44, s44, 0x1800
	s_addc_u32 s45, s45, 0
	global_load_lds_dwordx4 v78, s[44:45]
	v_mfma_f32_32x32x16_f16 a[0:15], v[48:51], v[0:3], a[0:15]
	ds_read_b128 v[24:27], v84 offset:59328
	ds_read_b128 v[48:51], v84 offset:65472
	s_waitcnt lgkmcnt(11)
	v_mfma_f32_32x32x16_f16 a[80:95], v[4:7], v[100:103], a[80:95]
	s_waitcnt lgkmcnt(9)
	v_mfma_f32_32x32x16_f16 a[64:79], v[8:11], v[100:103], a[64:79]
	s_waitcnt lgkmcnt(7)
	v_mfma_f32_32x32x16_f16 a[48:63], v[12:15], v[100:103], a[48:63]
	s_waitcnt lgkmcnt(5)
	v_mfma_f32_32x32x16_f16 a[32:47], v[16:19], v[100:103], a[32:47]
	s_waitcnt lgkmcnt(3)
	v_mfma_f32_32x32x16_f16 a[16:31], v[20:23], v[100:103], a[16:31]
	s_waitcnt lgkmcnt(1)
	v_mfma_f32_32x32x16_f16 a[0:15], v[24:27], v[100:103], a[0:15]
	s_waitcnt vmcnt(10)
	s_waitcnt lgkmcnt(0)
	s_barrier
	v_mfma_f32_32x32x16_f16 a[80:95], v[28:31], v[104:107], a[80:95]
	ds_read_b128 v[4:7], v98
	ds_read_b128 v[28:31], v98 offset:6144
	s_add_u32 m0, s46, 0xd3c0
	s_add_u32 s40, s40, 0x1800
	s_addc_u32 s41, s41, 0
	global_load_lds_dwordx4 v76, s[40:41]
	v_mfma_f32_32x32x16_f16 a[64:79], v[32:35], v[104:107], a[64:79]
	ds_read_b128 v[8:11], v98 offset:1024
	ds_read_b128 v[32:35], v98 offset:7168
	v_mfma_f32_32x32x16_f16 a[48:63], v[36:39], v[104:107], a[48:63]
	ds_read_b128 v[12:15], v98 offset:2048
	ds_read_b128 v[36:39], v98 offset:8192
	s_add_u32 m0, s47, 0xd3c0
	s_add_u32 s42, s42, 0x1800
	s_addc_u32 s43, s43, 0
	global_load_lds_dwordx4 v77, s[42:43]
	v_mfma_f32_32x32x16_f16 a[32:47], v[40:43], v[104:107], a[32:47]
	ds_read_b128 v[16:19], v98 offset:3072
	ds_read_b128 v[40:43], v98 offset:9216
	v_mfma_f32_32x32x16_f16 a[16:31], v[44:47], v[104:107], a[16:31]
	ds_read_b128 v[20:23], v98 offset:4096
	ds_read_b128 v[44:47], v98 offset:10240
	s_add_u32 m0, s48, 0xd3c0
	s_add_u32 s44, s44, 0x1800
	s_addc_u32 s45, s45, 0
	global_load_lds_dwordx4 v78, s[44:45]
	v_mfma_f32_32x32x16_f16 a[0:15], v[48:51], v[104:107], a[0:15]
	ds_read_b128 v[24:27], v98 offset:5120
	ds_read_b128 v[48:51], v98 offset:11264
	s_waitcnt lgkmcnt(11)
	v_mfma_f32_32x32x16_f16 a[80:95], v[4:7], v[108:111], a[80:95]
	s_waitcnt vmcnt(26)
	ds_write_b128 v81, v[116:119]
	ds_write_b128 v81, v[120:123] offset:1024
	ds_write_b128 v81, v[124:127] offset:2048
	ds_write_b128 v81, v[128:131] offset:3072
	s_waitcnt lgkmcnt(13)
	v_mfma_f32_32x32x16_f16 a[64:79], v[8:11], v[108:111], a[64:79]
	ds_read_b128 v[52:55], v95
	ds_read_b128 v[56:59], v96
	s_waitcnt lgkmcnt(14)
	ds_read_b128 v[60:63], v97
	s_waitcnt lgkmcnt(14)
	ds_read_b128 v[0:3], v94
	v_mfma_f32_32x32x16_f16 a[48:63], v[12:15], v[108:111], a[48:63]
	global_load_dwordx4 v[116:119], v64, s[4:5] offset:1152
	global_load_dwordx4 v[120:123], v66, s[4:5] offset:1152
	global_load_dwordx4 v[124:127], v68, s[4:5] offset:1152
	global_load_dwordx4 v[128:131], v70, s[4:5] offset:1152
	s_waitcnt lgkmcnt(13)
	v_mfma_f32_32x32x16_f16 a[32:47], v[16:19], v[108:111], a[32:47]
	s_waitcnt lgkmcnt(11)
	v_mfma_f32_32x32x16_f16 a[16:31], v[20:23], v[108:111], a[16:31]
	s_waitcnt lgkmcnt(9)
	v_mfma_f32_32x32x16_f16 a[0:15], v[24:27], v[108:111], a[0:15]
	s_waitcnt vmcnt(14)
	s_waitcnt lgkmcnt(0)
	s_barrier
	v_mfma_f32_32x32x16_f16 a[80:95], v[28:31], v[112:115], a[80:95]
	ds_read_b128 v[4:7], v84 offset:0
	ds_read_b128 v[28:31], v84 offset:6144
	s_add_u32 m0, s46, 0x103c0
	s_add_u32 s40, s40, 0x1800
	s_addc_u32 s41, s41, 0
	global_load_lds_dwordx4 v76, s[40:41]
	v_mfma_f32_32x32x16_f16 a[64:79], v[32:35], v[112:115], a[64:79]
	ds_read_b128 v[8:11], v84 offset:1024
	ds_read_b128 v[32:35], v84 offset:7168
	v_mfma_f32_32x32x16_f16 a[48:63], v[36:39], v[112:115], a[48:63]
	ds_read_b128 v[12:15], v84 offset:2048
	ds_read_b128 v[36:39], v84 offset:8192
	s_add_u32 m0, s47, 0x103c0
	s_add_u32 s42, s42, 0x1800
	s_addc_u32 s43, s43, 0
	global_load_lds_dwordx4 v77, s[42:43]
	v_mfma_f32_32x32x16_f16 a[32:47], v[40:43], v[112:115], a[32:47]
	ds_read_b128 v[16:19], v84 offset:3072
	ds_read_b128 v[40:43], v84 offset:9216
	v_mfma_f32_32x32x16_f16 a[16:31], v[44:47], v[112:115], a[16:31]
	ds_read_b128 v[20:23], v84 offset:4096
	ds_read_b128 v[44:47], v84 offset:10240
	s_add_u32 m0, s48, 0x103c0
	s_add_u32 s44, s44, 0x1800
	s_addc_u32 s45, s45, 0
	global_load_lds_dwordx4 v78, s[44:45]
	v_mfma_f32_32x32x16_f16 a[0:15], v[48:51], v[112:115], a[0:15]
	ds_read_b128 v[24:27], v84 offset:5120
	ds_read_b128 v[48:51], v84 offset:11264
	s_waitcnt lgkmcnt(11)
	v_mfma_f32_32x32x16_f16 a[80:95], v[4:7], v[52:55], a[80:95]
	s_waitcnt lgkmcnt(9)
	v_mfma_f32_32x32x16_f16 a[64:79], v[8:11], v[52:55], a[64:79]
	s_waitcnt lgkmcnt(7)
	v_mfma_f32_32x32x16_f16 a[48:63], v[12:15], v[52:55], a[48:63]
	s_waitcnt lgkmcnt(5)
	v_mfma_f32_32x32x16_f16 a[32:47], v[16:19], v[52:55], a[32:47]
	s_waitcnt lgkmcnt(3)
	v_mfma_f32_32x32x16_f16 a[16:31], v[20:23], v[52:55], a[16:31]
	s_waitcnt lgkmcnt(1)
	v_mfma_f32_32x32x16_f16 a[0:15], v[24:27], v[52:55], a[0:15]
	s_waitcnt vmcnt(10)
	s_waitcnt lgkmcnt(0)
	s_barrier
	v_mfma_f32_32x32x16_f16 a[80:95], v[28:31], v[56:59], a[80:95]
	ds_read_b128 v[4:7], v84 offset:12288
	ds_read_b128 v[28:31], v84 offset:18432
	s_add_u32 m0, s46, 0x0
	s_add_u32 s40, s40, 0x1800
	s_addc_u32 s41, s41, 0
	global_load_lds_dwordx4 v76, s[40:41]
	v_mfma_f32_32x32x16_f16 a[64:79], v[32:35], v[56:59], a[64:79]
	ds_read_b128 v[8:11], v84 offset:13312
	ds_read_b128 v[32:35], v84 offset:19456
	v_mfma_f32_32x32x16_f16 a[48:63], v[36:39], v[56:59], a[48:63]
	ds_read_b128 v[12:15], v84 offset:14336
	ds_read_b128 v[36:39], v84 offset:20480
	s_add_u32 m0, s47, 0x0
	s_add_u32 s42, s42, 0x1800
	s_addc_u32 s43, s43, 0
	global_load_lds_dwordx4 v77, s[42:43]
	v_mfma_f32_32x32x16_f16 a[32:47], v[40:43], v[56:59], a[32:47]
	ds_read_b128 v[16:19], v84 offset:15360
	ds_read_b128 v[40:43], v84 offset:21504
	v_mfma_f32_32x32x16_f16 a[16:31], v[44:47], v[56:59], a[16:31]
	ds_read_b128 v[20:23], v84 offset:16384
	ds_read_b128 v[44:47], v84 offset:22528
	s_add_u32 m0, s48, 0x0
	s_add_u32 s44, s44, 0x1800
	s_addc_u32 s45, s45, 0
	global_load_lds_dwordx4 v78, s[44:45]
	v_mfma_f32_32x32x16_f16 a[0:15], v[48:51], v[56:59], a[0:15]
	ds_read_b128 v[24:27], v84 offset:17408
	ds_read_b128 v[48:51], v84 offset:23552
	s_waitcnt lgkmcnt(11)
	v_mfma_f32_32x32x16_f16 a[80:95], v[4:7], v[60:63], a[80:95]
	s_waitcnt vmcnt(26)
	ds_write_b128 v81, v[132:135]
	ds_write_b128 v81, v[136:139] offset:1024
	ds_write_b128 v81, v[140:143] offset:2048
	ds_write_b128 v81, v[144:147] offset:3072
	s_waitcnt lgkmcnt(13)
	v_mfma_f32_32x32x16_f16 a[64:79], v[8:11], v[60:63], a[64:79]
	ds_read_b128 v[100:103], v95
	ds_read_b128 v[104:107], v96
	s_waitcnt lgkmcnt(14)
	ds_read_b128 v[108:111], v97
	s_waitcnt lgkmcnt(14)
	ds_read_b128 v[112:115], v94
	v_mfma_f32_32x32x16_f16 a[48:63], v[12:15], v[60:63], a[48:63]
	global_load_dwordx4 v[132:135], v64, s[4:5] offset:1280
	global_load_dwordx4 v[136:139], v66, s[4:5] offset:1280
	global_load_dwordx4 v[140:143], v68, s[4:5] offset:1280
	global_load_dwordx4 v[144:147], v70, s[4:5] offset:1280
	s_waitcnt lgkmcnt(13)
	v_mfma_f32_32x32x16_f16 a[32:47], v[16:19], v[60:63], a[32:47]
	s_waitcnt lgkmcnt(11)
	v_mfma_f32_32x32x16_f16 a[16:31], v[20:23], v[60:63], a[16:31]
	s_waitcnt lgkmcnt(9)
	v_mfma_f32_32x32x16_f16 a[0:15], v[24:27], v[60:63], a[0:15]
	s_waitcnt vmcnt(14)
	s_waitcnt lgkmcnt(0)
	s_barrier
	v_mfma_f32_32x32x16_f16 a[80:95], v[28:31], v[0:3], a[80:95]
	ds_read_b128 v[4:7], v84 offset:54208
	ds_read_b128 v[28:31], v84 offset:60352
	s_add_u32 m0, s46, 0x3000
	s_add_u32 s40, s40, 0x1800
	s_addc_u32 s41, s41, 0
	global_load_lds_dwordx4 v76, s[40:41]
	v_mfma_f32_32x32x16_f16 a[64:79], v[32:35], v[0:3], a[64:79]
	ds_read_b128 v[8:11], v84 offset:55232
	ds_read_b128 v[32:35], v84 offset:61376
	v_mfma_f32_32x32x16_f16 a[48:63], v[36:39], v[0:3], a[48:63]
	ds_read_b128 v[12:15], v84 offset:56256
	ds_read_b128 v[36:39], v84 offset:62400
	s_add_u32 m0, s47, 0x3000
	s_add_u32 s42, s42, 0x1800
	s_addc_u32 s43, s43, 0
	global_load_lds_dwordx4 v77, s[42:43]
	v_mfma_f32_32x32x16_f16 a[32:47], v[40:43], v[0:3], a[32:47]
	ds_read_b128 v[16:19], v84 offset:57280
	ds_read_b128 v[40:43], v84 offset:63424
	v_mfma_f32_32x32x16_f16 a[16:31], v[44:47], v[0:3], a[16:31]
	ds_read_b128 v[20:23], v84 offset:58304
	ds_read_b128 v[44:47], v84 offset:64448
	s_add_u32 m0, s48, 0x3000
	s_add_u32 s44, s44, 0x1800
	s_addc_u32 s45, s45, 0
	global_load_lds_dwordx4 v78, s[44:45]
	v_mfma_f32_32x32x16_f16 a[0:15], v[48:51], v[0:3], a[0:15]
	ds_read_b128 v[24:27], v84 offset:59328
	ds_read_b128 v[48:51], v84 offset:65472
	s_waitcnt lgkmcnt(11)
	v_mfma_f32_32x32x16_f16 a[80:95], v[4:7], v[100:103], a[80:95]
	s_waitcnt lgkmcnt(9)
	v_mfma_f32_32x32x16_f16 a[64:79], v[8:11], v[100:103], a[64:79]
	s_waitcnt lgkmcnt(7)
	v_mfma_f32_32x32x16_f16 a[48:63], v[12:15], v[100:103], a[48:63]
	s_waitcnt lgkmcnt(5)
	v_mfma_f32_32x32x16_f16 a[32:47], v[16:19], v[100:103], a[32:47]
	s_waitcnt lgkmcnt(3)
	v_mfma_f32_32x32x16_f16 a[16:31], v[20:23], v[100:103], a[16:31]
	s_waitcnt lgkmcnt(1)
	v_mfma_f32_32x32x16_f16 a[0:15], v[24:27], v[100:103], a[0:15]
	s_waitcnt vmcnt(10)
	s_waitcnt lgkmcnt(0)
	s_barrier
	v_mfma_f32_32x32x16_f16 a[80:95], v[28:31], v[104:107], a[80:95]
	ds_read_b128 v[4:7], v98
	ds_read_b128 v[28:31], v98 offset:6144
	s_add_u32 m0, s46, 0xd3c0
	s_add_u32 s40, s40, 0x1800
	s_addc_u32 s41, s41, 0
	global_load_lds_dwordx4 v76, s[40:41]
	v_mfma_f32_32x32x16_f16 a[64:79], v[32:35], v[104:107], a[64:79]
	ds_read_b128 v[8:11], v98 offset:1024
	ds_read_b128 v[32:35], v98 offset:7168
	v_mfma_f32_32x32x16_f16 a[48:63], v[36:39], v[104:107], a[48:63]
	ds_read_b128 v[12:15], v98 offset:2048
	ds_read_b128 v[36:39], v98 offset:8192
	s_add_u32 m0, s47, 0xd3c0
	s_add_u32 s42, s42, 0x1800
	s_addc_u32 s43, s43, 0
	global_load_lds_dwordx4 v77, s[42:43]
	v_mfma_f32_32x32x16_f16 a[32:47], v[40:43], v[104:107], a[32:47]
	ds_read_b128 v[16:19], v98 offset:3072
	ds_read_b128 v[40:43], v98 offset:9216
	v_mfma_f32_32x32x16_f16 a[16:31], v[44:47], v[104:107], a[16:31]
	ds_read_b128 v[20:23], v98 offset:4096
	ds_read_b128 v[44:47], v98 offset:10240
	s_add_u32 m0, s48, 0xd3c0
	s_add_u32 s44, s44, 0x1800
	s_addc_u32 s45, s45, 0
	global_load_lds_dwordx4 v78, s[44:45]
	v_mfma_f32_32x32x16_f16 a[0:15], v[48:51], v[104:107], a[0:15]
	ds_read_b128 v[24:27], v98 offset:5120
	ds_read_b128 v[48:51], v98 offset:11264
	s_waitcnt lgkmcnt(11)
	v_mfma_f32_32x32x16_f16 a[80:95], v[4:7], v[108:111], a[80:95]
	s_waitcnt vmcnt(26)
	ds_write_b128 v81, v[148:151]
	ds_write_b128 v81, v[152:155] offset:1024
	ds_write_b128 v81, v[156:159] offset:2048
	ds_write_b128 v81, v[72:75] offset:3072
	s_waitcnt lgkmcnt(13)
	v_mfma_f32_32x32x16_f16 a[64:79], v[8:11], v[108:111], a[64:79]
	ds_read_b128 v[52:55], v95
	ds_read_b128 v[56:59], v96
	s_waitcnt lgkmcnt(14)
	ds_read_b128 v[60:63], v97
	s_waitcnt lgkmcnt(14)
	ds_read_b128 v[0:3], v94
	v_mfma_f32_32x32x16_f16 a[48:63], v[12:15], v[108:111], a[48:63]
	global_load_dwordx4 v[148:151], v64, s[4:5] offset:1408
	global_load_dwordx4 v[152:155], v66, s[4:5] offset:1408
	global_load_dwordx4 v[156:159], v68, s[4:5] offset:1408
	global_load_dwordx4 v[72:75], v70, s[4:5] offset:1408
	s_waitcnt lgkmcnt(13)
	v_mfma_f32_32x32x16_f16 a[32:47], v[16:19], v[108:111], a[32:47]
	s_waitcnt lgkmcnt(11)
	v_mfma_f32_32x32x16_f16 a[16:31], v[20:23], v[108:111], a[16:31]
	s_waitcnt lgkmcnt(9)
	v_mfma_f32_32x32x16_f16 a[0:15], v[24:27], v[108:111], a[0:15]
	s_waitcnt vmcnt(14)
	s_waitcnt lgkmcnt(0)
	s_barrier
	v_mfma_f32_32x32x16_f16 a[80:95], v[28:31], v[112:115], a[80:95]
	ds_read_b128 v[4:7], v84 offset:0
	ds_read_b128 v[28:31], v84 offset:6144
	s_add_u32 m0, s46, 0x103c0
	s_add_u32 s40, s40, 0x1800
	s_addc_u32 s41, s41, 0
	global_load_lds_dwordx4 v76, s[40:41]
	v_mfma_f32_32x32x16_f16 a[64:79], v[32:35], v[112:115], a[64:79]
	ds_read_b128 v[8:11], v84 offset:1024
	ds_read_b128 v[32:35], v84 offset:7168
	v_mfma_f32_32x32x16_f16 a[48:63], v[36:39], v[112:115], a[48:63]
	ds_read_b128 v[12:15], v84 offset:2048
	ds_read_b128 v[36:39], v84 offset:8192
	s_add_u32 m0, s47, 0x103c0
	s_add_u32 s42, s42, 0x1800
	s_addc_u32 s43, s43, 0
	global_load_lds_dwordx4 v77, s[42:43]
	v_mfma_f32_32x32x16_f16 a[32:47], v[40:43], v[112:115], a[32:47]
	ds_read_b128 v[16:19], v84 offset:3072
	ds_read_b128 v[40:43], v84 offset:9216
	v_mfma_f32_32x32x16_f16 a[16:31], v[44:47], v[112:115], a[16:31]
	ds_read_b128 v[20:23], v84 offset:4096
	ds_read_b128 v[44:47], v84 offset:10240
	s_add_u32 m0, s48, 0x103c0
	s_add_u32 s44, s44, 0x1800
	s_addc_u32 s45, s45, 0
	global_load_lds_dwordx4 v78, s[44:45]
	v_mfma_f32_32x32x16_f16 a[0:15], v[48:51], v[112:115], a[0:15]
	ds_read_b128 v[24:27], v84 offset:5120
	ds_read_b128 v[48:51], v84 offset:11264
	s_waitcnt lgkmcnt(11)
	v_mfma_f32_32x32x16_f16 a[80:95], v[4:7], v[52:55], a[80:95]
	s_waitcnt lgkmcnt(9)
	v_mfma_f32_32x32x16_f16 a[64:79], v[8:11], v[52:55], a[64:79]
	s_waitcnt lgkmcnt(7)
	v_mfma_f32_32x32x16_f16 a[48:63], v[12:15], v[52:55], a[48:63]
	s_waitcnt lgkmcnt(5)
	v_mfma_f32_32x32x16_f16 a[32:47], v[16:19], v[52:55], a[32:47]
	s_waitcnt lgkmcnt(3)
	v_mfma_f32_32x32x16_f16 a[16:31], v[20:23], v[52:55], a[16:31]
	s_waitcnt lgkmcnt(1)
	v_mfma_f32_32x32x16_f16 a[0:15], v[24:27], v[52:55], a[0:15]
	s_waitcnt vmcnt(10)
	s_waitcnt lgkmcnt(0)
	s_barrier
	v_mfma_f32_32x32x16_f16 a[80:95], v[28:31], v[56:59], a[80:95]
	ds_read_b128 v[4:7], v84 offset:12288
	ds_read_b128 v[28:31], v84 offset:18432
	s_add_u32 m0, s46, 0x0
	s_add_u32 s40, s40, 0x1800
	s_addc_u32 s41, s41, 0
	global_load_lds_dwordx4 v76, s[40:41]
	v_mfma_f32_32x32x16_f16 a[64:79], v[32:35], v[56:59], a[64:79]
	ds_read_b128 v[8:11], v84 offset:13312
	ds_read_b128 v[32:35], v84 offset:19456
	v_mfma_f32_32x32x16_f16 a[48:63], v[36:39], v[56:59], a[48:63]
	ds_read_b128 v[12:15], v84 offset:14336
	ds_read_b128 v[36:39], v84 offset:20480
	s_add_u32 m0, s47, 0x0
	s_add_u32 s42, s42, 0x1800
	s_addc_u32 s43, s43, 0
	global_load_lds_dwordx4 v77, s[42:43]
	v_mfma_f32_32x32x16_f16 a[32:47], v[40:43], v[56:59], a[32:47]
	ds_read_b128 v[16:19], v84 offset:15360
	ds_read_b128 v[40:43], v84 offset:21504
	v_mfma_f32_32x32x16_f16 a[16:31], v[44:47], v[56:59], a[16:31]
	ds_read_b128 v[20:23], v84 offset:16384
	ds_read_b128 v[44:47], v84 offset:22528
	s_add_u32 m0, s48, 0x0
	s_add_u32 s44, s44, 0x1800
	s_addc_u32 s45, s45, 0
	global_load_lds_dwordx4 v78, s[44:45]
	v_mfma_f32_32x32x16_f16 a[0:15], v[48:51], v[56:59], a[0:15]
	ds_read_b128 v[24:27], v84 offset:17408
	ds_read_b128 v[48:51], v84 offset:23552
	s_waitcnt lgkmcnt(11)
	v_mfma_f32_32x32x16_f16 a[80:95], v[4:7], v[60:63], a[80:95]
	s_waitcnt vmcnt(26)
	ds_write_b128 v81, v[116:119]
	ds_write_b128 v81, v[120:123] offset:1024
	ds_write_b128 v81, v[124:127] offset:2048
	ds_write_b128 v81, v[128:131] offset:3072
	s_waitcnt lgkmcnt(13)
	v_mfma_f32_32x32x16_f16 a[64:79], v[8:11], v[60:63], a[64:79]
	ds_read_b128 v[100:103], v95
	ds_read_b128 v[104:107], v96
	s_waitcnt lgkmcnt(14)
	ds_read_b128 v[108:111], v97
	s_waitcnt lgkmcnt(14)
	ds_read_b128 v[112:115], v94
	v_mfma_f32_32x32x16_f16 a[48:63], v[12:15], v[60:63], a[48:63]
	global_load_dwordx4 v[116:119], v64, s[4:5] offset:1440
	global_load_dwordx4 v[120:123], v66, s[4:5] offset:1440
	global_load_dwordx4 v[124:127], v68, s[4:5] offset:1440
	global_load_dwordx4 v[128:131], v70, s[4:5] offset:1440
	s_waitcnt lgkmcnt(13)
	v_mfma_f32_32x32x16_f16 a[32:47], v[16:19], v[60:63], a[32:47]
	s_waitcnt lgkmcnt(11)
	v_mfma_f32_32x32x16_f16 a[16:31], v[20:23], v[60:63], a[16:31]
	s_waitcnt lgkmcnt(9)
	v_mfma_f32_32x32x16_f16 a[0:15], v[24:27], v[60:63], a[0:15]
	s_waitcnt vmcnt(14)
	s_waitcnt lgkmcnt(0)
	s_barrier
	v_mfma_f32_32x32x16_f16 a[80:95], v[28:31], v[0:3], a[80:95]
	ds_read_b128 v[4:7], v84 offset:54208
	ds_read_b128 v[28:31], v84 offset:60352
	s_add_u32 m0, s46, 0x3000
	s_add_u32 s40, s40, 0x1800
	s_addc_u32 s41, s41, 0
	global_load_lds_dwordx4 v76, s[40:41]
	v_mfma_f32_32x32x16_f16 a[64:79], v[32:35], v[0:3], a[64:79]
	ds_read_b128 v[8:11], v84 offset:55232
	ds_read_b128 v[32:35], v84 offset:61376
	v_mfma_f32_32x32x16_f16 a[48:63], v[36:39], v[0:3], a[48:63]
	ds_read_b128 v[12:15], v84 offset:56256
	ds_read_b128 v[36:39], v84 offset:62400
	s_add_u32 m0, s47, 0x3000
	s_add_u32 s42, s42, 0x1800
	s_addc_u32 s43, s43, 0
	global_load_lds_dwordx4 v77, s[42:43]
	v_mfma_f32_32x32x16_f16 a[32:47], v[40:43], v[0:3], a[32:47]
	ds_read_b128 v[16:19], v84 offset:57280
	ds_read_b128 v[40:43], v84 offset:63424
	v_mfma_f32_32x32x16_f16 a[16:31], v[44:47], v[0:3], a[16:31]
	ds_read_b128 v[20:23], v84 offset:58304
	ds_read_b128 v[44:47], v84 offset:64448
	s_add_u32 m0, s48, 0x3000
	s_add_u32 s44, s44, 0x1800
	s_addc_u32 s45, s45, 0
	global_load_lds_dwordx4 v78, s[44:45]
	v_mfma_f32_32x32x16_f16 a[0:15], v[48:51], v[0:3], a[0:15]
	ds_read_b128 v[24:27], v84 offset:59328
	ds_read_b128 v[48:51], v84 offset:65472
	s_waitcnt lgkmcnt(11)
	v_mfma_f32_32x32x16_f16 a[80:95], v[4:7], v[100:103], a[80:95]
	s_waitcnt lgkmcnt(9)
	v_mfma_f32_32x32x16_f16 a[64:79], v[8:11], v[100:103], a[64:79]
	s_waitcnt lgkmcnt(7)
	v_mfma_f32_32x32x16_f16 a[48:63], v[12:15], v[100:103], a[48:63]
	s_waitcnt lgkmcnt(5)
	v_mfma_f32_32x32x16_f16 a[32:47], v[16:19], v[100:103], a[32:47]
	s_waitcnt lgkmcnt(3)
	v_mfma_f32_32x32x16_f16 a[16:31], v[20:23], v[100:103], a[16:31]
	s_waitcnt lgkmcnt(1)
	v_mfma_f32_32x32x16_f16 a[0:15], v[24:27], v[100:103], a[0:15]
	s_waitcnt vmcnt(10)
	s_waitcnt lgkmcnt(0)
	s_barrier
	v_mfma_f32_32x32x16_f16 a[80:95], v[28:31], v[104:107], a[80:95]
	ds_read_b128 v[4:7], v98
	ds_read_b128 v[28:31], v98 offset:6144
	s_add_u32 m0, s46, 0xd3c0
	s_add_u32 s40, s40, 0x1800
	s_addc_u32 s41, s41, 0
	global_load_lds_dwordx4 v76, s[40:41]
	v_mfma_f32_32x32x16_f16 a[64:79], v[32:35], v[104:107], a[64:79]
	ds_read_b128 v[8:11], v98 offset:1024
	ds_read_b128 v[32:35], v98 offset:7168
	v_mfma_f32_32x32x16_f16 a[48:63], v[36:39], v[104:107], a[48:63]
	ds_read_b128 v[12:15], v98 offset:2048
	ds_read_b128 v[36:39], v98 offset:8192
	s_add_u32 m0, s47, 0xd3c0
	s_add_u32 s42, s42, 0x1800
	s_addc_u32 s43, s43, 0
	global_load_lds_dwordx4 v77, s[42:43]
	v_mfma_f32_32x32x16_f16 a[32:47], v[40:43], v[104:107], a[32:47]
	ds_read_b128 v[16:19], v98 offset:3072
	ds_read_b128 v[40:43], v98 offset:9216
	v_mfma_f32_32x32x16_f16 a[16:31], v[44:47], v[104:107], a[16:31]
	ds_read_b128 v[20:23], v98 offset:4096
	ds_read_b128 v[44:47], v98 offset:10240
	s_add_u32 m0, s48, 0xd3c0
	s_add_u32 s44, s44, 0x1800
	s_addc_u32 s45, s45, 0
	global_load_lds_dwordx4 v78, s[44:45]
	v_mfma_f32_32x32x16_f16 a[0:15], v[48:51], v[104:107], a[0:15]
	ds_read_b128 v[24:27], v98 offset:5120
	ds_read_b128 v[48:51], v98 offset:11264
	s_waitcnt lgkmcnt(11)
	v_mfma_f32_32x32x16_f16 a[80:95], v[4:7], v[108:111], a[80:95]
	s_waitcnt vmcnt(26)
	ds_write_b128 v81, v[132:135]
	ds_write_b128 v81, v[136:139] offset:1024
	ds_write_b128 v81, v[140:143] offset:2048
	ds_write_b128 v81, v[144:147] offset:3072
	s_waitcnt lgkmcnt(13)
	v_mfma_f32_32x32x16_f16 a[64:79], v[8:11], v[108:111], a[64:79]
	ds_read_b128 v[52:55], v95
	ds_read_b128 v[56:59], v96
	s_waitcnt lgkmcnt(14)
	ds_read_b128 v[60:63], v97
	s_waitcnt lgkmcnt(14)
	ds_read_b128 v[0:3], v94
	v_mfma_f32_32x32x16_f16 a[48:63], v[12:15], v[108:111], a[48:63]
	s_waitcnt lgkmcnt(13)
	v_mfma_f32_32x32x16_f16 a[32:47], v[16:19], v[108:111], a[32:47]
	s_waitcnt lgkmcnt(11)
	v_mfma_f32_32x32x16_f16 a[16:31], v[20:23], v[108:111], a[16:31]
	s_waitcnt lgkmcnt(9)
	v_mfma_f32_32x32x16_f16 a[0:15], v[24:27], v[108:111], a[0:15]
	s_waitcnt vmcnt(10)
	s_waitcnt lgkmcnt(0)
	s_barrier
	v_mfma_f32_32x32x16_f16 a[80:95], v[28:31], v[112:115], a[80:95]
	ds_read_b128 v[4:7], v84 offset:0
	ds_read_b128 v[28:31], v84 offset:6144
	s_add_u32 m0, s46, 0x103c0
	s_add_u32 s40, s40, 0x1800
	s_addc_u32 s41, s41, 0
	global_load_lds_dwordx4 v76, s[40:41]
	v_mfma_f32_32x32x16_f16 a[64:79], v[32:35], v[112:115], a[64:79]
	ds_read_b128 v[8:11], v84 offset:1024
	ds_read_b128 v[32:35], v84 offset:7168
	v_mfma_f32_32x32x16_f16 a[48:63], v[36:39], v[112:115], a[48:63]
	ds_read_b128 v[12:15], v84 offset:2048
	ds_read_b128 v[36:39], v84 offset:8192
	s_add_u32 m0, s47, 0x103c0
	s_add_u32 s42, s42, 0x1800
	s_addc_u32 s43, s43, 0
	global_load_lds_dwordx4 v77, s[42:43]
	v_mfma_f32_32x32x16_f16 a[32:47], v[40:43], v[112:115], a[32:47]
	ds_read_b128 v[16:19], v84 offset:3072
	ds_read_b128 v[40:43], v84 offset:9216
	v_mfma_f32_32x32x16_f16 a[16:31], v[44:47], v[112:115], a[16:31]
	ds_read_b128 v[20:23], v84 offset:4096
	ds_read_b128 v[44:47], v84 offset:10240
	s_add_u32 m0, s48, 0x103c0
	s_add_u32 s44, s44, 0x1800
	s_addc_u32 s45, s45, 0
	global_load_lds_dwordx4 v78, s[44:45]
	v_mfma_f32_32x32x16_f16 a[0:15], v[48:51], v[112:115], a[0:15]
	ds_read_b128 v[24:27], v84 offset:5120
	ds_read_b128 v[48:51], v84 offset:11264
	s_waitcnt lgkmcnt(11)
	v_mfma_f32_32x32x16_f16 a[80:95], v[4:7], v[52:55], a[80:95]
	s_waitcnt lgkmcnt(9)
	v_mfma_f32_32x32x16_f16 a[64:79], v[8:11], v[52:55], a[64:79]
	s_waitcnt lgkmcnt(7)
	v_mfma_f32_32x32x16_f16 a[48:63], v[12:15], v[52:55], a[48:63]
	s_waitcnt lgkmcnt(5)
	v_mfma_f32_32x32x16_f16 a[32:47], v[16:19], v[52:55], a[32:47]
	s_waitcnt lgkmcnt(3)
	v_mfma_f32_32x32x16_f16 a[16:31], v[20:23], v[52:55], a[16:31]
	s_waitcnt lgkmcnt(1)
	v_mfma_f32_32x32x16_f16 a[0:15], v[24:27], v[52:55], a[0:15]
	s_waitcnt vmcnt(6)
	s_waitcnt lgkmcnt(0)
	s_barrier
	v_mfma_f32_32x32x16_f16 a[80:95], v[28:31], v[56:59], a[80:95]
	ds_read_b128 v[4:7], v84 offset:12288
	ds_read_b128 v[28:31], v84 offset:18432
	s_add_u32 m0, s46, 0x0
	s_add_u32 s40, s40, 0x1800
	s_addc_u32 s41, s41, 0
	global_load_lds_dwordx4 v76, s[40:41]
	v_mfma_f32_32x32x16_f16 a[64:79], v[32:35], v[56:59], a[64:79]
	ds_read_b128 v[8:11], v84 offset:13312
	ds_read_b128 v[32:35], v84 offset:19456
	v_mfma_f32_32x32x16_f16 a[48:63], v[36:39], v[56:59], a[48:63]
	ds_read_b128 v[12:15], v84 offset:14336
	ds_read_b128 v[36:39], v84 offset:20480
	s_add_u32 m0, s47, 0x0
	s_add_u32 s42, s42, s49
	s_addc_u32 s43, s43, 0
	global_load_lds_dwordx4 v77, s[42:43]
	v_mfma_f32_32x32x16_f16 a[32:47], v[40:43], v[56:59], a[32:47]
	ds_read_b128 v[16:19], v84 offset:15360
	ds_read_b128 v[40:43], v84 offset:21504
	v_mfma_f32_32x32x16_f16 a[16:31], v[44:47], v[56:59], a[16:31]
	ds_read_b128 v[20:23], v84 offset:16384
	ds_read_b128 v[44:47], v84 offset:22528
	s_add_u32 m0, s48, 0x0
	s_add_u32 s44, s44, 0xc00
	s_addc_u32 s45, s45, 0
	global_load_lds_dwordx4 v78, s[44:45]
	v_mfma_f32_32x32x16_f16 a[0:15], v[48:51], v[56:59], a[0:15]
	ds_read_b128 v[24:27], v84 offset:17408
	ds_read_b128 v[48:51], v84 offset:23552
	s_waitcnt lgkmcnt(11)
	v_mfma_f32_32x32x16_f16 a[80:95], v[4:7], v[60:63], a[80:95]
	s_waitcnt vmcnt(22)
	ds_write_b128 v81, v[148:151]
	ds_write_b128 v81, v[152:155] offset:1024
	ds_write_b128 v81, v[156:159] offset:2048
	ds_write_b128 v81, v[72:75] offset:3072
	s_waitcnt lgkmcnt(13)
	v_mfma_f32_32x32x16_f16 a[64:79], v[8:11], v[60:63], a[64:79]
	ds_read_b128 v[100:103], v95
	ds_read_b128 v[104:107], v96
	s_waitcnt lgkmcnt(14)
	ds_read_b128 v[108:111], v97
	s_waitcnt lgkmcnt(14)
	ds_read_b128 v[112:115], v94
	v_mfma_f32_32x32x16_f16 a[48:63], v[12:15], v[60:63], a[48:63]
	s_waitcnt lgkmcnt(13)
	v_mfma_f32_32x32x16_f16 a[32:47], v[16:19], v[60:63], a[32:47]
	s_waitcnt lgkmcnt(11)
	v_mfma_f32_32x32x16_f16 a[16:31], v[20:23], v[60:63], a[16:31]
	s_waitcnt lgkmcnt(9)
	v_mfma_f32_32x32x16_f16 a[0:15], v[24:27], v[60:63], a[0:15]
	s_waitcnt vmcnt(6)
	s_waitcnt lgkmcnt(0)
	s_barrier
	v_mfma_f32_32x32x16_f16 a[80:95], v[28:31], v[0:3], a[80:95]
	ds_read_b128 v[4:7], v84 offset:54208
	ds_read_b128 v[28:31], v84 offset:60352
	v_mfma_f32_32x32x16_f16 a[64:79], v[32:35], v[0:3], a[64:79]
	ds_read_b128 v[8:11], v84 offset:55232
	ds_read_b128 v[32:35], v84 offset:61376
	v_mfma_f32_32x32x16_f16 a[48:63], v[36:39], v[0:3], a[48:63]
	ds_read_b128 v[12:15], v84 offset:56256
	ds_read_b128 v[36:39], v84 offset:62400
	v_mfma_f32_32x32x16_f16 a[32:47], v[40:43], v[0:3], a[32:47]
	ds_read_b128 v[16:19], v84 offset:57280
	ds_read_b128 v[40:43], v84 offset:63424
	v_mfma_f32_32x32x16_f16 a[16:31], v[44:47], v[0:3], a[16:31]
	ds_read_b128 v[20:23], v84 offset:58304
	ds_read_b128 v[44:47], v84 offset:64448
	v_mfma_f32_32x32x16_f16 a[0:15], v[48:51], v[0:3], a[0:15]
	ds_read_b128 v[24:27], v84 offset:59328
	ds_read_b128 v[48:51], v84 offset:65472
	s_waitcnt lgkmcnt(11)
	v_mfma_f32_32x32x16_f16 a[80:95], v[4:7], v[100:103], a[80:95]
	s_waitcnt lgkmcnt(9)
	v_mfma_f32_32x32x16_f16 a[64:79], v[8:11], v[100:103], a[64:79]
	s_waitcnt lgkmcnt(7)
	v_mfma_f32_32x32x16_f16 a[48:63], v[12:15], v[100:103], a[48:63]
	s_waitcnt lgkmcnt(5)
	v_mfma_f32_32x32x16_f16 a[32:47], v[16:19], v[100:103], a[32:47]
	s_waitcnt lgkmcnt(3)
	v_mfma_f32_32x32x16_f16 a[16:31], v[20:23], v[100:103], a[16:31]
	s_waitcnt lgkmcnt(1)
	v_mfma_f32_32x32x16_f16 a[0:15], v[24:27], v[100:103], a[0:15]
	s_waitcnt vmcnt(3)
	s_waitcnt lgkmcnt(0)
	s_barrier
	v_mfma_f32_32x32x16_f16 a[80:95], v[28:31], v[104:107], a[80:95]
	ds_read_b128 v[4:7], v98
	ds_read_b128 v[28:31], v98 offset:6144
	v_mfma_f32_32x32x16_f16 a[64:79], v[32:35], v[104:107], a[64:79]
	ds_read_b128 v[8:11], v98 offset:1024
	ds_read_b128 v[32:35], v98 offset:7168
	v_mfma_f32_32x32x16_f16 a[48:63], v[36:39], v[104:107], a[48:63]
	ds_read_b128 v[12:15], v98 offset:2048
	ds_read_b128 v[36:39], v98 offset:8192
	v_mfma_f32_32x32x16_f16 a[32:47], v[40:43], v[104:107], a[32:47]
	ds_read_b128 v[16:19], v98 offset:3072
	ds_read_b128 v[40:43], v98 offset:9216
	v_mfma_f32_32x32x16_f16 a[16:31], v[44:47], v[104:107], a[16:31]
	ds_read_b128 v[20:23], v98 offset:4096
	ds_read_b128 v[44:47], v98 offset:10240
	v_mfma_f32_32x32x16_f16 a[0:15], v[48:51], v[104:107], a[0:15]
	ds_read_b128 v[24:27], v98 offset:5120
	ds_read_b128 v[48:51], v98 offset:11264
	s_waitcnt lgkmcnt(11)
	v_mfma_f32_32x32x16_f16 a[80:95], v[4:7], v[108:111], a[80:95]
	s_waitcnt vmcnt(12)
	ds_write_b128 v81, v[116:119]
	ds_write_b128 v81, v[120:123] offset:1024
	ds_write_b128 v81, v[124:127] offset:2048
	ds_write_b128 v81, v[128:131] offset:3072
	s_waitcnt lgkmcnt(13)
	v_mfma_f32_32x32x16_f16 a[64:79], v[8:11], v[108:111], a[64:79]
	ds_read_b128 v[0:3], v94
	s_waitcnt lgkmcnt(12)
	v_mfma_f32_32x32x16_f16 a[48:63], v[12:15], v[108:111], a[48:63]
	s_waitcnt lgkmcnt(10)
	v_mfma_f32_32x32x16_f16 a[32:47], v[16:19], v[108:111], a[32:47]
	s_waitcnt lgkmcnt(8)
	v_mfma_f32_32x32x16_f16 a[16:31], v[20:23], v[108:111], a[16:31]
	s_waitcnt lgkmcnt(6)
	v_mfma_f32_32x32x16_f16 a[0:15], v[24:27], v[108:111], a[0:15]
	s_waitcnt vmcnt(0)
	s_waitcnt lgkmcnt(0)
	s_barrier
	v_mfma_f32_32x32x16_f16 a[80:95], v[28:31], v[112:115], a[80:95]
	ds_read_b128 v[4:7], v84 offset:0
	v_mfma_f32_32x32x16_f16 a[64:79], v[32:35], v[112:115], a[64:79]
	ds_read_b128 v[8:11], v84 offset:1024
	v_mfma_f32_32x32x16_f16 a[48:63], v[36:39], v[112:115], a[48:63]
	ds_read_b128 v[12:15], v84 offset:2048
	v_mfma_f32_32x32x16_f16 a[32:47], v[40:43], v[112:115], a[32:47]
	ds_read_b128 v[16:19], v84 offset:3072
	v_mfma_f32_32x32x16_f16 a[16:31], v[44:47], v[112:115], a[16:31]
	ds_read_b128 v[20:23], v84 offset:4096
	v_mfma_f32_32x32x16_f16 a[0:15], v[48:51], v[112:115], a[0:15]
	ds_read_b128 v[24:27], v84 offset:5120
	s_waitcnt lgkmcnt(0)
	v_mfma_f32_32x32x16_f16 a[80:95], v[4:7], v[0:3], a[80:95]
	v_mfma_f32_32x32x16_f16 a[16:31], v[20:23], v[0:3], a[16:31]
	v_lshlrev_b32_e32 v22, 4, v85
	v_mfma_f32_32x32x16_f16 a[64:79], v[8:11], v[0:3], a[64:79]
	v_mfma_f32_32x32x16_f16 a[48:63], v[12:15], v[0:3], a[48:63]
	s_nop 7
	v_accvgpr_read_b32 v13, a88
	v_mfma_f32_32x32x16_f16 a[32:47], v[16:19], v[0:3], a[32:47]
	v_accvgpr_read_b32 v17, a92
	v_mfma_f32_32x32x16_f16 a[0:15], v[24:27], v[0:3], a[0:15]
	ds_read_b128 v[2:5], v22 offset:53248
	ds_read_b128 v[6:9], v22 offset:53280
	v_accvgpr_read_b32 v1, a80
	v_lshlrev_b32_e32 v0, 4, v92
	s_waitcnt lgkmcnt(1)
	v_add_f32_e32 v1, v1, v2
	v_accvgpr_read_b32 v2, a81
	v_add_f32_e32 v2, v3, v2
	v_max_f32_e32 v10, 0, v2
	v_accvgpr_read_b32 v2, a82
	v_add_f32_e32 v2, v4, v2
	v_max_f32_e32 v11, 0, v2
	v_accvgpr_read_b32 v2, a83
	v_add_f32_e32 v2, v5, v2
	v_max_f32_e32 v12, 0, v2
	v_accvgpr_read_b32 v2, a84
	s_waitcnt lgkmcnt(0)
	v_add_f32_e32 v2, v2, v6
	v_max_f32_e32 v6, 0, v2
	v_accvgpr_read_b32 v2, a85
	v_add_f32_e32 v2, v7, v2
	v_max_f32_e32 v7, 0, v2
	v_accvgpr_read_b32 v2, a86
	v_add_f32_e32 v2, v8, v2
	v_max_f32_e32 v8, 0, v2
	v_accvgpr_read_b32 v2, a87
	v_add_f32_e32 v2, v9, v2
	v_max_f32_e32 v9, 0, v2
	ds_read_b128 v[2:5], v22 offset:53312
	v_max_f32_e32 v1, 0, v1
	s_waitcnt lgkmcnt(0)
	v_add_f32_e32 v2, v13, v2
	v_max_f32_e32 v13, 0, v2
	v_accvgpr_read_b32 v2, a89
	v_add_f32_e32 v2, v3, v2
	v_max_f32_e32 v14, 0, v2
	v_accvgpr_read_b32 v2, a90
	v_add_f32_e32 v2, v4, v2
	v_max_f32_e32 v15, 0, v2
	v_accvgpr_read_b32 v2, a91
	v_add_f32_e32 v2, v5, v2
	v_max_f32_e32 v16, 0, v2
	ds_read_b128 v[2:5], v22 offset:53344
	s_waitcnt lgkmcnt(0)
	v_add_f32_e32 v2, v17, v2
	v_max_f32_e32 v17, 0, v2
	v_accvgpr_read_b32 v2, a93
	v_add_f32_e32 v2, v3, v2
	v_max_f32_e32 v18, 0, v2
	v_accvgpr_read_b32 v2, a94
	v_add_f32_e32 v2, v4, v2
	v_max_f32_e32 v19, 0, v2
	v_accvgpr_read_b32 v2, a95
	v_add_f32_e32 v2, v5, v2
	v_cvt_pk_f16_f32 v5, v8, v9
	v_cvt_pk_f16_f32 v4, v6, v7
	ds_read_b128 v[6:9], v0 offset:40960
	v_max_f32_e32 v20, 0, v2
	v_cvt_pk_f16_f32 v3, v11, v12
	v_cvt_pk_f16_f32 v2, v1, v10
	v_accvgpr_read_b32 v1, a64
	s_waitcnt lgkmcnt(0)
	v_mfma_f32_32x32x16_f16 a[80:95], v[6:9], v[2:5], 0
	ds_read_b128 v[6:9], v0 offset:41984
	v_cvt_pk_f16_f32 v5, v19, v20
	v_cvt_pk_f16_f32 v4, v17, v18
	v_cvt_pk_f16_f32 v3, v15, v16
	v_cvt_pk_f16_f32 v2, v13, v14
	v_accvgpr_read_b32 v13, a72
	v_accvgpr_read_b32 v17, a76
	s_waitcnt lgkmcnt(0)
	v_mfma_f32_32x32x16_f16 a[80:95], v[6:9], v[2:5], a[80:95]
	ds_read_b128 v[2:5], v22 offset:53376
	v_accvgpr_read_b32 v9, a68
	s_waitcnt lgkmcnt(0)
	v_add_f32_e32 v1, v1, v2
	v_accvgpr_read_b32 v2, a65
	v_add_f32_e32 v2, v3, v2
	v_max_f32_e32 v6, 0, v2
	v_accvgpr_read_b32 v2, a66
	v_add_f32_e32 v2, v4, v2
	v_max_f32_e32 v7, 0, v2
	v_accvgpr_read_b32 v2, a67
	v_add_f32_e32 v2, v5, v2
	v_max_f32_e32 v8, 0, v2
	ds_read_b128 v[2:5], v22 offset:53408
	v_max_f32_e32 v1, 0, v1
	s_waitcnt lgkmcnt(0)
	v_add_f32_e32 v2, v9, v2
	v_max_f32_e32 v9, 0, v2
	v_accvgpr_read_b32 v2, a69
	v_add_f32_e32 v2, v3, v2
	v_max_f32_e32 v10, 0, v2
	v_accvgpr_read_b32 v2, a70
	v_add_f32_e32 v2, v4, v2
	v_max_f32_e32 v11, 0, v2
	v_accvgpr_read_b32 v2, a71
	v_add_f32_e32 v2, v5, v2
	v_max_f32_e32 v12, 0, v2
	ds_read_b128 v[2:5], v22 offset:53440
	s_waitcnt lgkmcnt(0)
	v_add_f32_e32 v2, v13, v2
	v_max_f32_e32 v13, 0, v2
	v_accvgpr_read_b32 v2, a73
	v_add_f32_e32 v2, v3, v2
	v_max_f32_e32 v14, 0, v2
	v_accvgpr_read_b32 v2, a74
	v_add_f32_e32 v2, v4, v2
	v_max_f32_e32 v15, 0, v2
	v_accvgpr_read_b32 v2, a75
	v_add_f32_e32 v2, v5, v2
	v_max_f32_e32 v16, 0, v2
	ds_read_b128 v[2:5], v22 offset:53472
	s_waitcnt lgkmcnt(0)
	v_add_f32_e32 v2, v17, v2
	v_max_f32_e32 v17, 0, v2
	v_accvgpr_read_b32 v2, a77
	v_add_f32_e32 v2, v3, v2
	v_max_f32_e32 v18, 0, v2
	v_accvgpr_read_b32 v2, a78
	v_add_f32_e32 v2, v4, v2
	v_max_f32_e32 v19, 0, v2
	v_accvgpr_read_b32 v2, a79
	v_add_f32_e32 v2, v5, v2
	v_max_f32_e32 v20, 0, v2
	v_cvt_pk_f16_f32 v4, v9, v10
	v_cvt_pk_f16_f32 v3, v7, v8
	v_cvt_pk_f16_f32 v2, v1, v6
	ds_read_b128 v[6:9], v0 offset:43008
	v_cvt_pk_f16_f32 v5, v11, v12
	v_accvgpr_read_b32 v1, a48
	s_waitcnt lgkmcnt(0)
	v_mfma_f32_32x32x16_f16 a[80:95], v[6:9], v[2:5], a[80:95]
	ds_read_b128 v[6:9], v0 offset:44032
	v_cvt_pk_f16_f32 v5, v19, v20
	v_cvt_pk_f16_f32 v4, v17, v18
	v_cvt_pk_f16_f32 v3, v15, v16
	v_cvt_pk_f16_f32 v2, v13, v14
	v_accvgpr_read_b32 v13, a56
	v_accvgpr_read_b32 v17, a60
	s_waitcnt lgkmcnt(0)
	v_mfma_f32_32x32x16_f16 a[80:95], v[6:9], v[2:5], a[80:95]
	ds_read_b128 v[2:5], v22 offset:53504
	v_accvgpr_read_b32 v9, a52
	s_waitcnt lgkmcnt(0)
	v_add_f32_e32 v1, v1, v2
	v_accvgpr_read_b32 v2, a49
	v_add_f32_e32 v2, v3, v2
	v_max_f32_e32 v6, 0, v2
	v_accvgpr_read_b32 v2, a50
	v_add_f32_e32 v2, v4, v2
	v_max_f32_e32 v7, 0, v2
	v_accvgpr_read_b32 v2, a51
	v_add_f32_e32 v2, v5, v2
	v_max_f32_e32 v8, 0, v2
	ds_read_b128 v[2:5], v22 offset:53536
	v_max_f32_e32 v1, 0, v1
	s_waitcnt lgkmcnt(0)
	v_add_f32_e32 v2, v9, v2
	v_max_f32_e32 v9, 0, v2
	v_accvgpr_read_b32 v2, a53
	v_add_f32_e32 v2, v3, v2
	v_max_f32_e32 v10, 0, v2
	v_accvgpr_read_b32 v2, a54
	v_add_f32_e32 v2, v4, v2
	v_max_f32_e32 v11, 0, v2
	v_accvgpr_read_b32 v2, a55
	v_add_f32_e32 v2, v5, v2
	v_max_f32_e32 v12, 0, v2
	ds_read_b128 v[2:5], v22 offset:53568
	s_waitcnt lgkmcnt(0)
	v_add_f32_e32 v2, v13, v2
	v_max_f32_e32 v13, 0, v2
	v_accvgpr_read_b32 v2, a57
	v_add_f32_e32 v2, v3, v2
	v_max_f32_e32 v14, 0, v2
	v_accvgpr_read_b32 v2, a58
	v_add_f32_e32 v2, v4, v2
	v_max_f32_e32 v15, 0, v2
	v_accvgpr_read_b32 v2, a59
	v_add_f32_e32 v2, v5, v2
	v_max_f32_e32 v16, 0, v2
	ds_read_b128 v[2:5], v22 offset:53600
	s_waitcnt lgkmcnt(0)
	v_add_f32_e32 v2, v17, v2
	v_max_f32_e32 v17, 0, v2
	v_accvgpr_read_b32 v2, a61
	v_add_f32_e32 v2, v3, v2
	v_max_f32_e32 v18, 0, v2
	v_accvgpr_read_b32 v2, a62
	v_add_f32_e32 v2, v4, v2
	v_max_f32_e32 v19, 0, v2
	v_accvgpr_read_b32 v2, a63
	v_add_f32_e32 v2, v5, v2
	v_max_f32_e32 v20, 0, v2
	v_cvt_pk_f16_f32 v4, v9, v10
	v_cvt_pk_f16_f32 v3, v7, v8
	v_cvt_pk_f16_f32 v2, v1, v6
	ds_read_b128 v[6:9], v0 offset:45056
	v_cvt_pk_f16_f32 v5, v11, v12
	v_accvgpr_read_b32 v1, a32
	s_waitcnt lgkmcnt(0)
	v_mfma_f32_32x32x16_f16 a[80:95], v[6:9], v[2:5], a[80:95]
	ds_read_b128 v[6:9], v0 offset:46080
	v_cvt_pk_f16_f32 v5, v19, v20
	v_cvt_pk_f16_f32 v4, v17, v18
	v_cvt_pk_f16_f32 v3, v15, v16
	v_cvt_pk_f16_f32 v2, v13, v14
	v_accvgpr_read_b32 v13, a40
	v_accvgpr_read_b32 v17, a44
	s_waitcnt lgkmcnt(0)
	v_mfma_f32_32x32x16_f16 a[80:95], v[6:9], v[2:5], a[80:95]
	ds_read_b128 v[2:5], v22 offset:53632
	v_accvgpr_read_b32 v9, a36
	s_waitcnt lgkmcnt(0)
	v_add_f32_e32 v1, v1, v2
	v_accvgpr_read_b32 v2, a33
	v_add_f32_e32 v2, v3, v2
	v_max_f32_e32 v6, 0, v2
	v_accvgpr_read_b32 v2, a34
	v_add_f32_e32 v2, v4, v2
	v_max_f32_e32 v7, 0, v2
	v_accvgpr_read_b32 v2, a35
	v_add_f32_e32 v2, v5, v2
	v_max_f32_e32 v8, 0, v2
	ds_read_b128 v[2:5], v22 offset:53664
	v_max_f32_e32 v1, 0, v1
	s_waitcnt lgkmcnt(0)
	v_add_f32_e32 v2, v9, v2
	v_max_f32_e32 v9, 0, v2
	v_accvgpr_read_b32 v2, a37
	v_add_f32_e32 v2, v3, v2
	v_max_f32_e32 v10, 0, v2
	v_accvgpr_read_b32 v2, a38
	v_add_f32_e32 v2, v4, v2
	v_max_f32_e32 v11, 0, v2
	v_accvgpr_read_b32 v2, a39
	v_add_f32_e32 v2, v5, v2
	v_max_f32_e32 v12, 0, v2
	ds_read_b128 v[2:5], v22 offset:53696
	s_waitcnt lgkmcnt(0)
	v_add_f32_e32 v2, v13, v2
	v_max_f32_e32 v13, 0, v2
	v_accvgpr_read_b32 v2, a41
	v_add_f32_e32 v2, v3, v2
	v_max_f32_e32 v14, 0, v2
	v_accvgpr_read_b32 v2, a42
	v_add_f32_e32 v2, v4, v2
	v_max_f32_e32 v15, 0, v2
	v_accvgpr_read_b32 v2, a43
	v_add_f32_e32 v2, v5, v2
	v_max_f32_e32 v16, 0, v2
	ds_read_b128 v[2:5], v22 offset:53728
	s_waitcnt lgkmcnt(0)
	v_add_f32_e32 v2, v17, v2
	v_max_f32_e32 v17, 0, v2
	v_accvgpr_read_b32 v2, a45
	v_add_f32_e32 v2, v3, v2
	v_max_f32_e32 v18, 0, v2
	v_accvgpr_read_b32 v2, a46
	v_add_f32_e32 v2, v4, v2
	v_max_f32_e32 v19, 0, v2
	v_accvgpr_read_b32 v2, a47
	v_add_f32_e32 v2, v5, v2
	v_max_f32_e32 v20, 0, v2
	v_cvt_pk_f16_f32 v4, v9, v10
	v_cvt_pk_f16_f32 v3, v7, v8
	v_cvt_pk_f16_f32 v2, v1, v6
	ds_read_b128 v[6:9], v0 offset:47104
	v_cvt_pk_f16_f32 v5, v11, v12
	v_accvgpr_read_b32 v1, a16
	s_waitcnt lgkmcnt(0)
	v_mfma_f32_32x32x16_f16 a[32:47], v[6:9], v[2:5], 0
	ds_read_b128 v[6:9], v0 offset:48128
	v_cvt_pk_f16_f32 v5, v19, v20
	v_cvt_pk_f16_f32 v4, v17, v18
	v_cvt_pk_f16_f32 v3, v15, v16
	v_cvt_pk_f16_f32 v2, v13, v14
	v_accvgpr_read_b32 v13, a24
	v_accvgpr_read_b32 v17, a28
	s_waitcnt lgkmcnt(0)
	v_mfma_f32_32x32x16_f16 a[32:47], v[6:9], v[2:5], a[32:47]
	ds_read_b128 v[2:5], v22 offset:53760
	v_accvgpr_read_b32 v9, a20
	s_waitcnt lgkmcnt(0)
	v_add_f32_e32 v1, v1, v2
	v_accvgpr_read_b32 v2, a17
	v_add_f32_e32 v2, v3, v2
	v_max_f32_e32 v6, 0, v2
	v_accvgpr_read_b32 v2, a18
	v_add_f32_e32 v2, v4, v2
	v_max_f32_e32 v7, 0, v2
	v_accvgpr_read_b32 v2, a19
	v_add_f32_e32 v2, v5, v2
	v_max_f32_e32 v8, 0, v2
	ds_read_b128 v[2:5], v22 offset:53792
	v_max_f32_e32 v1, 0, v1
	s_waitcnt lgkmcnt(0)
	v_add_f32_e32 v2, v9, v2
	v_max_f32_e32 v9, 0, v2
	v_accvgpr_read_b32 v2, a21
	v_add_f32_e32 v2, v3, v2
	v_max_f32_e32 v10, 0, v2
	v_accvgpr_read_b32 v2, a22
	v_add_f32_e32 v2, v4, v2
	v_max_f32_e32 v11, 0, v2
	v_accvgpr_read_b32 v2, a23
	v_add_f32_e32 v2, v5, v2
	v_max_f32_e32 v12, 0, v2
	ds_read_b128 v[2:5], v22 offset:53824
	s_waitcnt lgkmcnt(0)
	v_add_f32_e32 v2, v13, v2
	v_max_f32_e32 v13, 0, v2
	v_accvgpr_read_b32 v2, a25
	v_add_f32_e32 v2, v3, v2
	v_max_f32_e32 v14, 0, v2
	v_accvgpr_read_b32 v2, a26
	v_add_f32_e32 v2, v4, v2
	v_max_f32_e32 v15, 0, v2
	v_accvgpr_read_b32 v2, a27
	v_add_f32_e32 v2, v5, v2
	v_max_f32_e32 v16, 0, v2
	ds_read_b128 v[2:5], v22 offset:53856
	s_waitcnt lgkmcnt(0)
	v_add_f32_e32 v2, v17, v2
	v_max_f32_e32 v17, 0, v2
	v_accvgpr_read_b32 v2, a29
	v_add_f32_e32 v2, v3, v2
	v_max_f32_e32 v18, 0, v2
	v_accvgpr_read_b32 v2, a30
	v_add_f32_e32 v2, v4, v2
	v_max_f32_e32 v19, 0, v2
	v_accvgpr_read_b32 v2, a31
	v_add_f32_e32 v2, v5, v2
	v_max_f32_e32 v20, 0, v2
	v_cvt_pk_f16_f32 v4, v9, v10
	v_cvt_pk_f16_f32 v3, v7, v8
	v_cvt_pk_f16_f32 v2, v1, v6
	ds_read_b128 v[6:9], v0 offset:49152
	v_cvt_pk_f16_f32 v5, v11, v12
	v_accvgpr_read_b32 v1, a0
	s_waitcnt lgkmcnt(0)
	v_mfma_f32_32x32x16_f16 a[32:47], v[6:9], v[2:5], a[32:47]
	ds_read_b128 v[6:9], v0 offset:50176
	v_cvt_pk_f16_f32 v5, v19, v20
	v_cvt_pk_f16_f32 v4, v17, v18
	v_cvt_pk_f16_f32 v3, v15, v16
	v_cvt_pk_f16_f32 v2, v13, v14
	v_accvgpr_read_b32 v13, a8
	v_accvgpr_read_b32 v17, a12
	s_waitcnt lgkmcnt(0)
	v_mfma_f32_32x32x16_f16 a[32:47], v[6:9], v[2:5], a[32:47]
	ds_read_b128 v[2:5], v22 offset:53888
	v_accvgpr_read_b32 v9, a4
	s_waitcnt lgkmcnt(0)
	v_add_f32_e32 v1, v1, v2
	v_accvgpr_read_b32 v2, a1
	v_add_f32_e32 v2, v3, v2
	v_max_f32_e32 v6, 0, v2
	v_accvgpr_read_b32 v2, a2
	v_add_f32_e32 v2, v4, v2
	v_max_f32_e32 v7, 0, v2
	v_accvgpr_read_b32 v2, a3
	v_add_f32_e32 v2, v5, v2
	v_max_f32_e32 v8, 0, v2
	ds_read_b128 v[2:5], v22 offset:53920
	v_max_f32_e32 v1, 0, v1
	s_waitcnt lgkmcnt(0)
	v_add_f32_e32 v2, v9, v2
	v_max_f32_e32 v9, 0, v2
	v_accvgpr_read_b32 v2, a5
	v_add_f32_e32 v2, v3, v2
	v_max_f32_e32 v10, 0, v2
	v_accvgpr_read_b32 v2, a6
	v_add_f32_e32 v2, v4, v2
	v_max_f32_e32 v11, 0, v2
	v_accvgpr_read_b32 v2, a7
	v_add_f32_e32 v2, v5, v2
	v_max_f32_e32 v12, 0, v2
	ds_read_b128 v[2:5], v22 offset:53952
	s_waitcnt lgkmcnt(0)
	v_add_f32_e32 v2, v13, v2
	v_max_f32_e32 v13, 0, v2
	v_accvgpr_read_b32 v2, a9
	v_add_f32_e32 v2, v3, v2
	v_max_f32_e32 v14, 0, v2
	v_accvgpr_read_b32 v2, a10
	v_add_f32_e32 v2, v4, v2
	v_max_f32_e32 v15, 0, v2
	v_accvgpr_read_b32 v2, a11
	v_add_f32_e32 v2, v5, v2
	v_max_f32_e32 v16, 0, v2
	ds_read_b128 v[2:5], v22 offset:53984
	s_waitcnt lgkmcnt(0)
	v_add_f32_e32 v2, v17, v2
	v_max_f32_e32 v17, 0, v2
	v_accvgpr_read_b32 v2, a13
	v_add_f32_e32 v2, v3, v2
	v_max_f32_e32 v18, 0, v2
	v_accvgpr_read_b32 v2, a14
	v_add_f32_e32 v2, v4, v2
	v_max_f32_e32 v19, 0, v2
	v_accvgpr_read_b32 v2, a15
	v_add_f32_e32 v2, v5, v2
	v_max_f32_e32 v20, 0, v2
	v_cvt_pk_f16_f32 v4, v9, v10
	v_cvt_pk_f16_f32 v3, v7, v8
	v_cvt_pk_f16_f32 v2, v1, v6
	ds_read_b128 v[6:9], v0 offset:51200
	v_cvt_pk_f16_f32 v5, v11, v12
	s_waitcnt lgkmcnt(0)
	s_nop 0
	v_mfma_f32_32x32x16_f16 a[32:47], v[6:9], v[2:5], a[32:47]
	ds_read_b128 v[6:9], v0 offset:52224
	v_cvt_pk_f16_f32 v5, v19, v20
	v_cvt_pk_f16_f32 v4, v17, v18
	v_cvt_pk_f16_f32 v3, v15, v16
	v_cvt_pk_f16_f32 v2, v13, v14
	s_waitcnt lgkmcnt(0)
	s_nop 0
	v_mfma_f32_32x32x16_f16 a[32:47], v[6:9], v[2:5], a[32:47]
	s_and_saveexec_b64 s[2:3], s[0:1]
	s_cbranch_execz .LBB3_39
	v_accvgpr_read_b32 v0, a80
	v_accvgpr_read_b32 v6, a86
	v_accvgpr_read_b32 v7, a87
	v_accvgpr_read_b32 v8, a88
	v_accvgpr_read_b32 v9, a89
	v_accvgpr_read_b32 v10, a90
	v_accvgpr_read_b32 v11, a91
	v_accvgpr_read_b32 v12, a92
	v_accvgpr_read_b32 v13, a93
	v_accvgpr_read_b32 v14, a94
	v_accvgpr_read_b32 v15, a95
	v_accvgpr_read_b32 v6, a32
	v_accvgpr_read_b32 v14, a40
	v_accvgpr_read_b32 v15, a41
	v_accvgpr_read_b32 v16, a42
	v_accvgpr_read_b32 v17, a43
	v_accvgpr_read_b32 v18, a44
	v_accvgpr_read_b32 v19, a45
	v_accvgpr_read_b32 v20, a46
	v_accvgpr_read_b32 v21, a47
	ds_read_b128 v[14:17], v22 offset:54016
	ds_read_b128 v[18:21], v22 offset:54080
	v_accvgpr_read_b32 v12, a38
	v_accvgpr_read_b32 v13, a39
	v_lshlrev_b32_e32 v24, 2, v85
	v_accvgpr_read_b32 v1, a81
	v_accvgpr_read_b32 v7, a33
	v_mad_i64_i32 v[12:13], s[0:1], v80, 40, s[18:19]
	v_ashrrev_i32_e32 v25, 31, v24
	v_accvgpr_read_b32 v3, a83
	v_accvgpr_read_b32 v9, a35
	v_lshl_add_u64 v[22:23], v[24:25], 2, v[12:13]
	v_mov_b32_e32 v25, v1
	s_waitcnt lgkmcnt(1)
	v_mov_b32_e32 v27, v15
	v_mov_b32_e32 v1, v7
	s_waitcnt lgkmcnt(0)
	v_mov_b32_e32 v15, v19
	v_accvgpr_read_b32 v2, a82
	v_accvgpr_read_b32 v8, a34
	v_pk_add_f32 v[0:1], v[0:1], v[14:15]
	v_mov_b32_e32 v7, v3
	v_mov_b32_e32 v15, v17
	v_mov_b32_e32 v3, v9
	v_mov_b32_e32 v17, v21
	v_mov_b32_e32 v24, v6
	v_mov_b32_e32 v26, v18
	v_mov_b32_e32 v6, v8
	v_mov_b32_e32 v14, v20
	v_pk_add_f32 v[2:3], v[2:3], v[16:17]
	v_pk_add_f32 v[24:25], v[24:25], v[26:27]
	s_waitcnt vmcnt(0)
	v_pk_mul_f32 v[0:1], v[82:83], v[0:1]
	v_pk_add_f32 v[6:7], v[6:7], v[14:15]
	v_pk_mul_f32 v[2:3], v[82:83], v[2:3]
	v_accvgpr_read_b32 v4, a84
	v_accvgpr_read_b32 v5, a85
	v_accvgpr_read_b32 v10, a36
	v_accvgpr_read_b32 v11, a37
	v_pk_fma_f32 v[0:1], v[82:83], v[24:25], v[0:1] op_sel:[1,0,0] op_sel_hi:[0,1,1]
	v_pk_fma_f32 v[2:3], v[82:83], v[6:7], v[2:3] op_sel:[1,0,0] op_sel_hi:[0,1,1]
	v_cmp_eq_u32_e32 vcc, 0, v85
	global_store_dwordx4 v[22:23], v[0:3], off
	s_and_b64 exec, exec, vcc
	s_cbranch_execz .LBB3_39
	s_mov_b32 s0, 0xd000
	v_add_u32_e64 v0, s0, 0
	ds_read2_b64 v[0:3], v0 offset0:100 offset1:108
	v_mov_b32_e32 v9, v5
	v_mov_b32_e32 v5, v11
	v_mov_b32_e32 v8, v10
	v_pk_mov_b32 v[6:7], v[82:83], v[82:83] op_sel:[1,0]
	s_waitcnt lgkmcnt(0)
	v_mov_b32_e32 v15, v1
	v_mov_b32_e32 v1, v3
	v_mov_b32_e32 v14, v2
	v_pk_add_f32 v[0:1], v[4:5], v[0:1]
	v_pk_add_f32 v[8:9], v[8:9], v[14:15]
	v_pk_mul_f32 v[0:1], v[82:83], v[0:1]
	s_nop 0
	v_pk_fma_f32 v[0:1], v[6:7], v[8:9], v[0:1]
	global_store_dwordx2 v[12:13], v[0:1], off offset:32
